# v026 + ph6: LayerNorm gamma/beta staged once per phase in wave-private LDS (ds_read_b128 instead of 16 global loads per trip), INFO prefetch 12 bytes, no vmcnt wait behind the row prefetch
# speedup vs baseline: 1.0138x; 1.0138x over previous
; __global__ void __launch_bounds__(NWAVES * 64, 2) mk_fwd(Args args) {
;     ...
;             auto tok_of = [&](int t0, int j) { return (j == 0 || t0 + NGW >= T) ? t0 : t0 + NGW; };
;             auto load_raw = [&](int t0) { return INFO[(size_t)tok_of(t0, (lane >> 2) & 1) * 4 + (lane & 3)]; };
;             auto unpack_raw = [&](const i32x4& raw, int (&e)[2][4], int (&p)[2][4], float (&gq)[2][4]) {
; #pragma unroll
;                 for (int j = 0; j < 2; ++j)
; #pragma unroll
;                     for (int k = 0; k < 4; ++k) { e[j][k] = __builtin_amdgcn_readlane(raw.x, 4 * j + k); p[j][k] = __builtin_amdgcn_readlane(raw.y, 4 * j + k);
;                         gq[j][k] = __int_as_float(__builtin_amdgcn_readlane(raw.z, 4 * j + k)) * (1.0f / 16.0f); } };
;             auto load_rows = [&](int t0, const int (&e)[2][4], const int (&p)[2][4], u32x4 (&xr)[2][2], u32x2 (&yr)[2][4][2]) {
; #pragma unroll
;                 for (int j = 0; j < 2; ++j) { const int t = tok_of(t0, j);
;                     xr[j][0] = *(const u32x4*)(YB + (size_t)t * D + 8 * lane); xr[j][1] = *(const u32x4*)(YB + (size_t)t * D + 512 + 8 * lane);
; #pragma unroll
;                     for (int k = 0; k < 4; ++k) { const unsigned char* yp = (const unsigned char*)YS + ((size_t)TB[e[j][k]] * 256 + p[j][k]) * D;
;                         yr[j][k][0] = *(const u32x2*)(yp + 8 * lane); yr[j][k][1] = *(const u32x2*)(yp + 512 + 8 * lane); } } };
;             u32x4 xr[2][2], xrn[2][2]; u32x2 yr[2][4][2], yrn[2][4][2]; float gt[2][4];
;             i32x4 raw = load_raw(gw);
;             { int e0[2][4], p0[2][4]; unpack_raw(raw, e0, p0, gt); load_rows(gw, e0, p0, xr, yr); }
;             raw = load_raw((gw + 2 * NGW < T) ? gw + 2 * NGW : gw);
.LBB0_704:
	s_mov_b32 s2, -1
	s_waitcnt lgkmcnt(0)
	s_barrier
	v_readlane_b32 s4, v253, 57
	v_mbcnt_lo_u32_b32 v0, s2, 0
	v_mbcnt_hi_u32_b32 v0, s2, v0
	s_nop 0
	v_and_b32_e32 v1, 4, v0
	v_cmp_eq_u32_e64 s[2:3], 0, v1
	v_mov_b32_e32 v1, s4
	v_readlane_b32 s4, v253, 19
	v_readlane_b32 s5, v253, 20
	s_nop 0
	v_mov_b32_e32 v2, s4
	v_readlane_b32 s4, v253, 52
	v_readlane_b32 s5, v253, 53
	s_or_b64 vcc, s[2:3], s[4:5]
	v_cndmask_b32_e32 v2, v1, v2, vcc
	v_ashrrev_i32_e32 v3, 31, v2
	v_readlane_b32 s4, v252, 39
	v_and_b32_e32 v1, 3, v0
	v_lshlrev_b64 v[2:3], 6, v[2:3]
	v_readlane_b32 s5, v252, 40
	v_lshlrev_b32_e32 v32, 4, v1
	s_cmp_lg_u32 s66, 3
	v_lshl_add_u64 v[2:3], s[4:5], 0, v[2:3]
	v_lshl_add_u64 v[2:3], v[2:3], 0, v[32:33]
	global_load_dwordx4 v[2:5], v[2:3], off nt
	v_readlane_b32 s4, v254, 38
	v_readlane_b32 s5, v254, 39
	s_cselect_b64 s[8:9], -1, 0
	s_andn2_b64 vcc, exec, s[4:5]
	s_waitcnt vmcnt(0)
	v_readlane_b32 s7, v2, 0
	v_readlane_b32 s6, v3, 0
	v_readlane_b32 s24, v4, 0
	v_readlane_b32 s11, v2, 1
	v_readlane_b32 s10, v3, 1
	v_readlane_b32 s25, v4, 1
	v_readlane_b32 s13, v2, 2
	v_readlane_b32 s12, v3, 2
	v_readlane_b32 s26, v4, 2
	v_readlane_b32 s15, v2, 3
	v_readlane_b32 s14, v3, 3
	v_readlane_b32 s27, v4, 3
	v_readlane_b32 s17, v2, 4
	v_readlane_b32 s16, v3, 4
	v_readlane_b32 s28, v4, 4
	v_readlane_b32 s19, v2, 5
	v_readlane_b32 s18, v3, 5
	v_readlane_b32 s29, v4, 5
	v_readlane_b32 s21, v2, 6
	v_readlane_b32 s20, v3, 6
	v_readlane_b32 s30, v4, 6
	v_readlane_b32 s23, v2, 7
	v_readlane_b32 s22, v3, 7
	v_readlane_b32 s31, v4, 7
	s_cbranch_vccnz .LBB0_719
	v_readlane_b32 s4, v254, 40
	v_readlane_b32 s5, v254, 41
	s_or_b32 s68, s4, 0x400
	s_mov_b64 s[34:35], s[84:85]
	v_readlane_b32 s80, v252, 43
	s_lshl_b64 s[4:5], s[68:69], 2
	v_readlane_b32 s84, v252, 47
	v_readlane_b32 s85, v252, 48
	v_readlane_b32 s94, v252, 57
	v_readlane_b32 s95, v252, 58
	s_mov_b64 s[84:85], s[34:35]
	s_add_u32 s34, s94, s4
	s_addc_u32 s35, s95, s5
	v_readlane_b32 s40, v252, 0
	v_lshlrev_b32_e32 v94, 3, v0
	v_readlane_b32 s41, v252, 1
	s_add_u32 s4, s40, s4
	v_ashrrev_i32_e32 v95, 31, v94
	s_addc_u32 s5, s41, s5
	v_lshlrev_b64 v[2:3], 2, v[94:95]
	v_lshl_add_u64 v[104:105], s[4:5], 0, v[2:3]
	v_readlane_b32 s4, v254, 13
	v_lshl_add_u64 v[102:103], s[34:35], 0, v[2:3]
	v_lshlrev_b64 v[20:21], 1, v[94:95]
	v_readlane_b32 s5, v254, 14
	v_readlane_b32 s34, v253, 60
	v_readlane_b32 s33, v253, 59
	v_lshl_add_u64 v[106:107], s[4:5], 0, v[20:21]
	v_cmp_eq_u32_e64 s[4:5], 0, v0
	v_readlane_b32 s35, v253, 61
	v_mov_b32_e32 v0, s33
	v_readlane_b32 s33, v253, 58
	s_or_b64 vcc, s[2:3], s[34:35]
	v_readlane_b32 s40, v252, 39
	v_mov_b32_e32 v1, s33
	v_cndmask_b32_e32 v0, v0, v1, vcc
	v_readlane_b32 s44, v254, 48
	v_ashrrev_i32_e32 v1, 31, v0
	v_readlane_b32 s41, v252, 40
	v_readlane_b32 s45, v254, 49
	v_lshlrev_b64 v[0:1], 6, v[0:1]
	v_lshl_add_u64 v[0:1], s[40:41], 0, v[0:1]
	v_lshl_add_u64 v[98:99], s[44:45], 0, v[2:3]
	v_readlane_b32 s44, v254, 44
	v_readlane_b32 s42, v252, 2
	v_readlane_b32 s43, v252, 3
	v_readlane_b32 s45, v254, 45
	v_lshl_add_u64 v[0:1], v[0:1], 0, v[32:33]
	s_lshl_b32 s23, s23, 2
	v_lshl_add_u64 v[100:101], s[44:45], 0, v[2:3]
	v_lshl_add_u64 v[110:111], s[42:43], 0, v[2:3]
	global_load_dwordx4 v[0:3], v[0:1], off nt
	s_add_i32 s23, s67, s23
	s_waitcnt vmcnt(0)
	v_mov_b32_e32 v3, s23
	ds_read_b32 v4, v3
	s_ashr_i32 s23, s22, 31
	s_lshl_b64 s[22:23], s[22:23], 10
	s_lshl_b32 s21, s21, 2
	s_add_i32 s21, s67, s21
	s_waitcnt lgkmcnt(0)
	v_ashrrev_i32_e32 v5, 31, v4
	v_lshlrev_b64 v[4:5], 18, v[4:5]
	v_lshl_add_u64 v[4:5], s[52:53], 0, v[4:5]
	v_lshl_add_u64 v[4:5], v[4:5], 0, s[22:23]
	v_lshl_add_u64 v[4:5], v[4:5], 0, v[94:95]
	v_mov_b32_e32 v3, s21
	global_load_dwordx2 v[112:113], v[4:5], off offset:512 nt
	global_load_dwordx2 v[114:115], v[4:5], off nt
	ds_read_b32 v4, v3
	s_ashr_i32 s21, s20, 31
	s_lshl_b64 s[20:21], s[20:21], 10
	s_lshl_b32 s19, s19, 2
	s_add_i32 s19, s67, s19
	s_waitcnt lgkmcnt(0)
	v_ashrrev_i32_e32 v5, 31, v4
	v_lshlrev_b64 v[4:5], 18, v[4:5]
	v_lshl_add_u64 v[4:5], s[52:53], 0, v[4:5]
	v_lshl_add_u64 v[4:5], v[4:5], 0, s[20:21]
	v_lshl_add_u64 v[4:5], v[4:5], 0, v[94:95]
	v_mov_b32_e32 v3, s19
	global_load_dwordx2 v[116:117], v[4:5], off offset:512 nt
	global_load_dwordx2 v[118:119], v[4:5], off nt
	ds_read_b32 v4, v3
	s_ashr_i32 s19, s18, 31
	s_lshl_b64 s[18:19], s[18:19], 10
	s_lshl_b32 s17, s17, 2
	s_add_i32 s17, s67, s17
	s_waitcnt lgkmcnt(0)
	v_ashrrev_i32_e32 v5, 31, v4
	v_lshlrev_b64 v[4:5], 18, v[4:5]
	v_lshl_add_u64 v[4:5], s[52:53], 0, v[4:5]
	v_lshl_add_u64 v[4:5], v[4:5], 0, s[18:19]
	v_lshl_add_u64 v[4:5], v[4:5], 0, v[94:95]
	v_mov_b32_e32 v3, s17
	global_load_dwordx2 v[120:121], v[4:5], off offset:512 nt
	global_load_dwordx2 v[122:123], v[4:5], off nt
	ds_read_b32 v4, v3
	s_ashr_i32 s17, s16, 31
	s_lshl_b64 s[16:17], s[16:17], 10
	s_lshl_b32 s15, s15, 2
	s_add_i32 s15, s67, s15
	s_waitcnt lgkmcnt(0)
; __global__ void __launch_bounds__(NWAVES * 64, 2) mk_fwd(Args args) {
;     ...
;             const float* lng = args.in[15] + (size_t)(layer * 2 + 1) * D; const float* lnb = args.in[16] + (size_t)(layer * 2 + 1) * D;
;             const float* lng1 = args.in[15] + (size_t)(layer * 2 + 0) * D; const float* lnb1 = args.in[16] + (size_t)(layer * 2 + 0) * D;
;     ...
;             auto load_rows = [&](int t0, const int (&e)[2][4], const int (&p)[2][4], u32x4 (&xr)[2][2], u32x2 (&yr)[2][4][2]) {
; #pragma unroll
;                 for (int j = 0; j < 2; ++j) { const int t = tok_of(t0, j);
;                     xr[j][0] = *(const u32x4*)(YB + (size_t)t * D + 8 * lane); xr[j][1] = *(const u32x4*)(YB + (size_t)t * D + 512 + 8 * lane);
; #pragma unroll
;                     for (int k = 0; k < 4; ++k) { const unsigned char* yp = (const unsigned char*)YS + ((size_t)TB[e[j][k]] * 256 + p[j][k]) * D;
;                         yr[j][k][0] = *(const u32x2*)(yp + 8 * lane); yr[j][k][1] = *(const u32x2*)(yp + 512 + 8 * lane); } } };
;             u32x4 xr[2][2], xrn[2][2]; u32x2 yr[2][4][2], yrn[2][4][2]; float gt[2][4];
;             i32x4 raw = load_raw(gw);
;             { int e0[2][4], p0[2][4]; unpack_raw(raw, e0, p0, gt); load_rows(gw, e0, p0, xr, yr); }
;             raw = load_raw((gw + 2 * NGW < T) ? gw + 2 * NGW : gw);
	v_ashrrev_i32_e32 v5, 31, v4
	v_lshlrev_b64 v[4:5], 18, v[4:5]
	v_lshl_add_u64 v[4:5], s[52:53], 0, v[4:5]
	v_lshl_add_u64 v[4:5], v[4:5], 0, s[16:17]
	v_readlane_b32 s16, v253, 54
	v_readlane_b32 s17, v253, 55
	v_lshl_add_u64 v[4:5], v[4:5], 0, v[94:95]
	v_mov_b32_e32 v3, s15
	v_lshl_add_u64 v[8:9], s[16:17], 0, v[20:21]
	global_load_dwordx2 v[132:133], v[4:5], off offset:512 nt
	global_load_dwordx2 v[134:135], v[4:5], off nt
	s_nop 0
	global_load_dwordx4 v[4:7], v[8:9], off offset:1024 nt
	s_nop 0
	global_load_dwordx4 v[8:11], v[8:9], off nt
	ds_read_b32 v12, v3
	s_ashr_i32 s15, s14, 31
	s_lshl_b64 s[14:15], s[14:15], 10
	s_lshl_b32 s13, s13, 2
	s_add_i32 s13, s67, s13
	s_waitcnt lgkmcnt(0)
	v_ashrrev_i32_e32 v13, 31, v12
	v_lshlrev_b64 v[12:13], 18, v[12:13]
	v_lshl_add_u64 v[12:13], s[52:53], 0, v[12:13]
	v_lshl_add_u64 v[12:13], v[12:13], 0, s[14:15]
	v_lshl_add_u64 v[12:13], v[12:13], 0, v[94:95]
	v_mov_b32_e32 v3, s13
	global_load_dwordx2 v[124:125], v[12:13], off offset:512 nt
	global_load_dwordx2 v[126:127], v[12:13], off nt
	ds_read_b32 v12, v3
	s_ashr_i32 s13, s12, 31
	s_lshl_b64 s[12:13], s[12:13], 10
	s_lshl_b32 s11, s11, 2
	s_add_i32 s11, s67, s11
	s_waitcnt lgkmcnt(0)
	v_ashrrev_i32_e32 v13, 31, v12
	v_lshlrev_b64 v[12:13], 18, v[12:13]
	v_lshl_add_u64 v[12:13], s[52:53], 0, v[12:13]
	v_lshl_add_u64 v[12:13], v[12:13], 0, s[12:13]
	v_lshl_add_u64 v[12:13], v[12:13], 0, v[94:95]
	v_mov_b32_e32 v3, s11
	global_load_dwordx2 v[128:129], v[12:13], off offset:512 nt
	global_load_dwordx2 v[130:131], v[12:13], off nt
	ds_read_b32 v12, v3
	s_ashr_i32 s11, s10, 31
	s_lshl_b64 s[10:11], s[10:11], 10
	s_lshl_b32 s7, s7, 2
	s_add_i32 s7, s67, s7
	s_waitcnt lgkmcnt(0)
	v_ashrrev_i32_e32 v13, 31, v12
	v_lshlrev_b64 v[12:13], 18, v[12:13]
	v_lshl_add_u64 v[12:13], s[52:53], 0, v[12:13]
	v_lshl_add_u64 v[12:13], v[12:13], 0, s[10:11]
	v_lshl_add_u64 v[12:13], v[12:13], 0, v[94:95]
	v_mov_b32_e32 v3, s7
	global_load_dwordx2 v[136:137], v[12:13], off offset:512 nt
	global_load_dwordx2 v[138:139], v[12:13], off nt
	ds_read_b32 v12, v3
	s_ashr_i32 s7, s6, 31
	s_lshl_b64 s[6:7], s[6:7], 10
	v_readlane_b32 s82, v252, 45
	v_readlane_b32 s83, v252, 46
	s_waitcnt lgkmcnt(0)
	v_ashrrev_i32_e32 v13, 31, v12
	v_lshlrev_b64 v[12:13], 18, v[12:13]
	v_lshl_add_u64 v[12:13], s[52:53], 0, v[12:13]
	v_lshl_add_u64 v[12:13], v[12:13], 0, s[6:7]
	v_readlane_b32 s6, v253, 50
	v_readlane_b32 s7, v253, 51
	v_lshl_add_u64 v[12:13], v[12:13], 0, v[94:95]
	global_load_dwordx2 v[142:143], v[12:13], off offset:512 nt
	global_load_dwordx2 v[144:145], v[12:13], off nt
	v_lshl_add_u64 v[16:17], s[6:7], 0, v[20:21]
	global_load_dwordx4 v[12:15], v[16:17], off offset:1024 nt
	s_nop 0
	global_load_dwordx4 v[16:19], v[16:17], off nt
	v_readlane_b32 s81, v252, 44
	v_readlane_b32 s88, v252, 51
	v_readlane_b32 s89, v252, 52
	v_readlane_b32 s92, v252, 55
	v_readlane_b32 s93, v252, 56
	v_readlane_b32 s82, v254, 9
	v_readlane_b32 s94, v254, 19
	v_readlane_b32 s80, v254, 17
	v_readlane_b32 s88, v254, 21
	v_readlane_b32 s92, v254, 15
	v_readlane_b32 s83, v254, 10
	v_readlane_b32 s95, v254, 20
	v_readlane_b32 s81, v254, 18
	v_readlane_b32 s89, v254, 22
	v_readlane_b32 s93, v254, 16
	v_readlane_b32 s83, v254, 23
	v_lshl_add_u64 v[96:97], s[40:41], 0, v[32:33]
	v_lshl_add_u64 v[108:109], s[36:37], 0, v[94:95]
	v_lshl_add_u64 v[140:141], s[94:95], 0, v[20:21]
	v_readlane_b32 s10, v253, 19
	v_readlane_b32 s86, v252, 49
	v_readlane_b32 s87, v252, 50
	v_readlane_b32 s90, v252, 53
	v_readlane_b32 s91, v252, 54
	v_readlane_b32 s11, v253, 20
	v_mbcnt_lo_u32_b32 v225, -1, 0
	v_mbcnt_hi_u32_b32 v225, -1, v225
	v_lshlrev_b32_e32 v225, 4, v225
	v_readlane_b32 s98, v252, 28
	s_lshl_b32 s98, s98, 14
	v_add_u32_e32 v225, s98, v225
	global_load_dwordx4 v[20:23], v[98:99], off offset:16
	global_load_dwordx4 v[24:27], v[98:99], off
	global_load_dwordx4 v[28:31], v[100:101], off
	global_load_dwordx4 v[36:39], v[100:101], off offset:16
	global_load_dwordx4 v[40:43], v[98:99], off offset:2048
	global_load_dwordx4 v[44:47], v[100:101], off offset:2048
	global_load_dwordx4 v[48:51], v[98:99], off offset:2064
	global_load_dwordx4 v[52:55], v[100:101], off offset:2064
	global_load_dwordx4 v[56:59], v[102:103], off offset:16
	global_load_dwordx4 v[60:63], v[102:103], off
	global_load_dwordx4 v[64:67], v[104:105], off offset:16
	global_load_dwordx4 v[68:71], v[104:105], off
	global_load_dwordx4 v[72:75], v[102:103], off offset:2064
	global_load_dwordx4 v[76:79], v[102:103], off offset:2048
	global_load_dwordx4 v[80:83], v[104:105], off offset:2064
	global_load_dwordx4 v[84:87], v[104:105], off offset:2048
	s_waitcnt vmcnt(0)
	ds_write_b128 v225, v[20:23]
	ds_write_b128 v225, v[24:27] offset:1024
	ds_write_b128 v225, v[28:31] offset:2048
	ds_write_b128 v225, v[36:39] offset:3072
	ds_write_b128 v225, v[40:43] offset:4096
	ds_write_b128 v225, v[44:47] offset:5120
	ds_write_b128 v225, v[48:51] offset:6144
	ds_write_b128 v225, v[52:55] offset:7168
	ds_write_b128 v225, v[56:59] offset:8192
	ds_write_b128 v225, v[60:63] offset:9216
	ds_write_b128 v225, v[64:67] offset:10240
	ds_write_b128 v225, v[68:71] offset:11264
	ds_write_b128 v225, v[72:75] offset:12288
	ds_write_b128 v225, v[76:79] offset:13312
	ds_write_b128 v225, v[80:83] offset:14336
	ds_write_b128 v225, v[84:87] offset:15360
	s_waitcnt lgkmcnt(0)
	s_branch .LBB0_707

; __global__ void __launch_bounds__(NWAVES * 64, 2) mk_fwd(Args args) {
;     ...
;             auto unpack_raw = [&](const i32x4& raw, int (&e)[2][4], int (&p)[2][4], float (&gq)[2][4]) {
; #pragma unroll
;                 for (int j = 0; j < 2; ++j)
; #pragma unroll
;                     for (int k = 0; k < 4; ++k) { e[j][k] = __builtin_amdgcn_readlane(raw.x, 4 * j + k); p[j][k] = __builtin_amdgcn_readlane(raw.y, 4 * j + k);
;                         gq[j][k] = __int_as_float(__builtin_amdgcn_readlane(raw.z, 4 * j + k)) * (1.0f / 16.0f); } };
;             auto load_rows = [&](int t0, const int (&e)[2][4], const int (&p)[2][4], u32x4 (&xr)[2][2], u32x2 (&yr)[2][4][2]) {
; #pragma unroll
;                 for (int j = 0; j < 2; ++j) { const int t = tok_of(t0, j);
;                     xr[j][0] = *(const u32x4*)(YB + (size_t)t * D + 8 * lane); xr[j][1] = *(const u32x4*)(YB + (size_t)t * D + 512 + 8 * lane);
; #pragma unroll
;                     for (int k = 0; k < 4; ++k) { const unsigned char* yp = (const unsigned char*)YS + ((size_t)TB[e[j][k]] * 256 + p[j][k]) * D;
;                         yr[j][k][0] = *(const u32x2*)(yp + 8 * lane); yr[j][k][1] = *(const u32x2*)(yp + 512 + 8 * lane); } } };
;     ...
;             for (int t0 = gw; t0 < T; t0 += 2 * NGW) {
;                 int tt[2]; tt[0] = t0; tt[1] = tok_of(t0, 1);
;                 const int t1 = (t0 + 2 * NGW < T) ? t0 + 2 * NGW : t0, t2 = (t1 + 2 * NGW < T) ? t1 + 2 * NGW : t1;
;                 int en[2][4], pn[2][4]; float gn[2][4];
;                 unpack_raw(raw, en, pn, gn);
;                 load_rows(t1, en, pn, xrn, yrn);
;                 raw = load_raw(t2);
.LBB0_707:
	v_readlane_b32 s7, v253, 56
	s_add_i32 s6, s7, s10
	s_cmp_lt_i32 s6, 0x8000
	s_cselect_b32 s18, s6, s10
	s_add_i32 s6, s18, s7
	s_cmp_lt_i32 s6, 0x8000
	s_cselect_b32 s11, s6, s18
	s_waitcnt vmcnt(0)
	v_readlane_b32 s7, v0, 0
	s_ashr_i32 s19, s18, 31
	s_lshl_b64 s[42:43], s[18:19], 11
	s_lshl_b32 s7, s7, 2
	v_mov_b64_e32 v[30:31], v[18:19]
	v_mov_b64_e32 v[36:37], v[14:15]
	v_readlane_b32 s34, v1, 0
	v_readlane_b32 s13, v0, 1
	v_readlane_b32 s40, v1, 1
	v_readlane_b32 s15, v0, 2
	v_readlane_b32 s22, v1, 2
	v_readlane_b32 s17, v0, 3
	v_readlane_b32 s20, v1, 3
	v_readlane_b32 s33, v0, 4
	v_readlane_b32 s16, v1, 4
	v_readlane_b32 s38, v0, 5
	v_readlane_b32 s14, v1, 5
	v_readlane_b32 s44, v0, 6
	v_readlane_b32 s12, v1, 6
	v_readlane_b32 s45, v0, 7
	v_readlane_b32 s6, v1, 7
	v_lshl_add_u64 v[0:1], v[140:141], 0, s[42:43]
	s_add_i32 s7, s67, s7
	v_mov_b64_e32 v[28:29], v[16:17]
	v_mov_b64_e32 v[34:35], v[12:13]
	global_load_dwordx4 v[16:19], v[0:1], off nt
	global_load_dwordx4 v[12:15], v[0:1], off offset:1024 nt
	v_mov_b32_e32 v0, s7
	s_lshl_b32 s7, s13, 2
	s_add_i32 s7, s67, s7
	v_mov_b32_e32 v1, s7
	s_lshl_b32 s7, s15, 2
	ds_read_b32 v0, v0
	s_add_i32 s7, s67, s7
	v_mov_b32_e32 v3, s7
	s_lshl_b32 s7, s17, 2
	v_mov_b64_e32 v[26:27], v[6:7]
	s_add_i32 s7, s67, s7
	v_mov_b64_e32 v[24:25], v[4:5]
	v_mul_f32_e32 v44, s24, v224
	v_mul_f32_e32 v42, s25, v224
	v_mul_f32_e32 v40, s26, v224
	v_mul_f32_e32 v38, s27, v224
	v_mul_f32_e32 v150, s28, v224
	v_mul_f32_e32 v148, s29, v224
	v_mul_f32_e32 v146, s30, v224
	v_mul_f32_e32 v32, s31, v224
	v_readlane_b32 s24, v2, 0
	v_readlane_b32 s25, v2, 1
	v_readlane_b32 s26, v2, 2
	v_readlane_b32 s27, v2, 3
	v_readlane_b32 s28, v2, 4
	v_readlane_b32 s29, v2, 5
	v_readlane_b32 s30, v2, 6
	v_readlane_b32 s31, v2, 7
	v_mov_b32_e32 v5, s7
	ds_read_b32 v2, v1
	ds_read_b32 v4, v3
	ds_read_b32 v6, v5
	s_waitcnt lgkmcnt(3)
	v_ashrrev_i32_e32 v1, 31, v0
	s_ashr_i32 s35, s34, 31
	v_lshlrev_b64 v[0:1], 18, v[0:1]
	s_waitcnt lgkmcnt(2)
	v_ashrrev_i32_e32 v3, 31, v2
	s_lshl_b64 s[34:35], s[34:35], 10
	v_lshl_add_u64 v[0:1], s[52:53], 0, v[0:1]
	s_ashr_i32 s41, s40, 31
	v_lshlrev_b64 v[2:3], 18, v[2:3]
	v_lshl_add_u64 v[0:1], v[0:1], 0, s[34:35]
	s_lshl_b64 s[34:35], s[40:41], 10
	v_lshl_add_u64 v[2:3], s[52:53], 0, v[2:3]
	s_ashr_i32 s23, s22, 31
	s_ashr_i32 s21, s20, 31
	v_lshl_add_u64 v[0:1], v[0:1], 0, v[94:95]
	v_lshl_add_u64 v[2:3], v[2:3], 0, s[34:35]
	s_waitcnt lgkmcnt(1)
	v_ashrrev_i32_e32 v5, 31, v4
	s_lshl_b64 s[22:23], s[22:23], 10
	s_lshl_b64 s[20:21], s[20:21], 10
	s_add_i32 s7, s18, s82
	v_mov_b64_e32 v[60:61], v[144:145]
	v_mov_b64_e32 v[52:53], v[142:143]
	v_mov_b64_e32 v[58:59], v[138:139]
	v_mov_b64_e32 v[50:51], v[136:137]
	v_lshl_add_u64 v[2:3], v[2:3], 0, v[94:95]
	global_load_dwordx2 v[144:145], v[0:1], off nt
	global_load_dwordx2 v[142:143], v[0:1], off offset:512 nt
	global_load_dwordx2 v[138:139], v[2:3], off nt
	global_load_dwordx2 v[136:137], v[2:3], off offset:512 nt
	v_lshlrev_b64 v[0:1], 18, v[4:5]
	s_waitcnt lgkmcnt(0)
	v_ashrrev_i32_e32 v7, 31, v6
	s_cmpk_gt_i32 s7, 0x7fff
	v_lshl_add_u64 v[0:1], s[52:53], 0, v[0:1]
	v_lshlrev_b64 v[2:3], 18, v[6:7]
	s_cselect_b32 s18, s18, s7
	v_lshl_add_u64 v[0:1], v[0:1], 0, s[22:23]
	v_lshl_add_u64 v[2:3], s[52:53], 0, v[2:3]
	s_ashr_i32 s19, s18, 31
	v_lshl_add_u64 v[0:1], v[0:1], 0, v[94:95]
	v_lshl_add_u64 v[2:3], v[2:3], 0, s[20:21]
	s_lshl_b64 s[18:19], s[18:19], 11
	s_lshl_b32 s7, s33, 2
	v_mov_b64_e32 v[56:57], v[130:131]
	v_mov_b64_e32 v[48:49], v[128:129]
	v_mov_b64_e32 v[54:55], v[126:127]
	v_mov_b64_e32 v[46:47], v[124:125]
	v_mov_b64_e32 v[22:23], v[10:11]
	v_lshl_add_u64 v[2:3], v[2:3], 0, v[94:95]
	global_load_dwordx2 v[130:131], v[0:1], off nt
	global_load_dwordx2 v[128:129], v[0:1], off offset:512 nt
	global_load_dwordx2 v[126:127], v[2:3], off nt
	global_load_dwordx2 v[124:125], v[2:3], off offset:512 nt
	v_lshl_add_u64 v[0:1], v[140:141], 0, s[18:19]
	s_add_i32 s7, s67, s7
	v_mov_b64_e32 v[20:21], v[8:9]
	global_load_dwordx4 v[8:11], v[0:1], off nt
	global_load_dwordx4 v[4:7], v[0:1], off offset:1024 nt
	v_mov_b32_e32 v0, s7
	s_lshl_b32 s7, s38, 2
	s_add_i32 s7, s67, s7
	v_mov_b32_e32 v1, s7
	s_lshl_b32 s7, s44, 2
	ds_read_b32 v0, v0
	s_add_i32 s7, s67, s7
	v_mov_b32_e32 v3, s7
	s_lshl_b32 s7, s45, 2
	s_add_i32 s7, s67, s7
	v_mov_b32_e32 v39, s7
	ds_read_b32 v2, v1
	ds_read_b32 v62, v3
	ds_read_b32 v64, v39
	s_waitcnt lgkmcnt(3)
	v_ashrrev_i32_e32 v1, 31, v0
	s_ashr_i32 s17, s16, 31
	v_lshlrev_b64 v[0:1], 18, v[0:1]
	s_waitcnt lgkmcnt(2)
	v_ashrrev_i32_e32 v3, 31, v2
	s_lshl_b64 s[16:17], s[16:17], 10
	v_lshl_add_u64 v[0:1], s[52:53], 0, v[0:1]
	s_ashr_i32 s15, s14, 31
	v_lshlrev_b64 v[2:3], 18, v[2:3]
	v_lshl_add_u64 v[0:1], v[0:1], 0, s[16:17]
	s_lshl_b64 s[14:15], s[14:15], 10
	v_lshl_add_u64 v[2:3], s[52:53], 0, v[2:3]
	v_lshl_add_u64 v[0:1], v[0:1], 0, v[94:95]
	v_lshl_add_u64 v[2:3], v[2:3], 0, s[14:15]
	s_waitcnt lgkmcnt(1)
	v_ashrrev_i32_e32 v63, 31, v62
	v_mov_b64_e32 v[166:167], v[134:135]
	v_mov_b64_e32 v[158:159], v[132:133]
	v_mov_b64_e32 v[164:165], v[122:123]
	v_mov_b64_e32 v[156:157], v[120:121]
	v_lshl_add_u64 v[2:3], v[2:3], 0, v[94:95]
	global_load_dwordx2 v[134:135], v[0:1], off nt
	global_load_dwordx2 v[132:133], v[0:1], off offset:512 nt
	global_load_dwordx2 v[122:123], v[2:3], off nt
	global_load_dwordx2 v[120:121], v[2:3], off offset:512 nt
	s_ashr_i32 s13, s12, 31
	v_lshlrev_b64 v[0:1], 18, v[62:63]
	s_lshl_b64 s[12:13], s[12:13], 10
	v_lshl_add_u64 v[0:1], s[52:53], 0, v[0:1]
	s_waitcnt lgkmcnt(0)
; __device__ __forceinline__ void unpack8(const u32x4 w, float (&f)[8]) { f[0] = bf_lo(w.x); f[1] = bf_hi(w.x); f[2] = bf_lo(w.y); f[3] = bf_hi(w.y); f[4] = bf_lo(w.z); f[5] = bf_hi(w.z); f[6] = bf_lo(w.w); f[7] = bf_hi(w.w); }
; __device__ __forceinline__ float wave_sum(float v) { v += dpp_f<0xB1>(v); v += dpp_f<0x4E>(v); v += dpp_f<0x141>(v); v += dpp_f<0x140>(v); v += xor_sw<16>(v); return sum_x32(v); }
; __device__ __forceinline__ void ln_row16(float (&v)[16], const float* lng, const float* lnb, int lane, float (&o)[16]) {
;     const float s = ((v[0] + v[1]) + (v[2] + v[3])) + ((v[4] + v[5]) + (v[6] + v[7])) + (((v[8] + v[9]) + (v[10] + v[11])) + ((v[12] + v[13]) + (v[14] + v[15])));
;     const float mean = wave_sum(s) * (1.0f / D);
; #pragma unroll
;     for (int i = 0; i < 16; ++i) v[i] -= mean;
;     const float s2 = ((v[0] * v[0] + v[1] * v[1]) + (v[2] * v[2] + v[3] * v[3])) + ((v[4] * v[4] + v[5] * v[5]) + (v[6] * v[6] + v[7] * v[7]))
;                    + (((v[8] * v[8] + v[9] * v[9]) + (v[10] * v[10] + v[11] * v[11])) + ((v[12] * v[12] + v[13] * v[13]) + (v[14] * v[14] + v[15] * v[15])));
;     const float rstd = 1.0f / sqrtf(wave_sum(s2) * (1.0f / D) + LN_EPS);
; #pragma unroll
;     for (int hf = 0; hf < 2; ++hf) { const int col = 512 * hf + 8 * lane;
;         const f32x4 g0 = *(const f32x4*)(lng + col), g1 = *(const f32x4*)(lng + col + 4), b0 = *(const f32x4*)(lnb + col), b1 = *(const f32x4*)(lnb + col + 4);
; __global__ void __launch_bounds__(NWAVES * 64, 2) mk_fwd(Args args) {
;     ...
;                 raw = load_raw(t2);
;                 __builtin_amdgcn_sched_barrier(0);
;                 float o[2][16];
; #pragma unroll
;                 for (int j = 0; j < 2; ++j) {
;                     float v[16], x1[16];
; #pragma unroll
;                     for (int hf = 0; hf < 2; ++hf) { float f[8]; unpack8(xr[j][hf], f);
; #pragma unroll
;                         for (int i = 0; i < 8; ++i) v[8 * hf + i] = f[i]; }
;                     ln_row16(v, lng1, lnb1, lane, x1);
	v_ashrrev_i32_e32 v65, 31, v64
	s_ashr_i32 s7, s6, 31
	v_lshl_add_u64 v[0:1], v[0:1], 0, s[12:13]
	v_lshlrev_b64 v[2:3], 18, v[64:65]
	s_lshl_b64 s[6:7], s[6:7], 10
	s_add_i32 s12, s11, s82
	v_lshl_add_u64 v[2:3], s[52:53], 0, v[2:3]
	s_cmpk_gt_i32 s12, 0x7fff
	v_lshl_add_u64 v[0:1], v[0:1], 0, v[94:95]
	v_lshl_add_u64 v[2:3], v[2:3], 0, s[6:7]
	s_cselect_b64 s[6:7], -1, 0
	v_mov_b64_e32 v[162:163], v[118:119]
	v_mov_b64_e32 v[154:155], v[116:117]
	v_mov_b64_e32 v[160:161], v[114:115]
	v_mov_b64_e32 v[152:153], v[112:113]
	v_lshl_add_u64 v[2:3], v[2:3], 0, v[94:95]
	global_load_dwordx2 v[118:119], v[0:1], off nt
	global_load_dwordx2 v[116:117], v[0:1], off offset:512 nt
	global_load_dwordx2 v[114:115], v[2:3], off nt
	global_load_dwordx2 v[112:113], v[2:3], off offset:512 nt
	v_mov_b32_e32 v0, s12
	v_mov_b32_e32 v1, s11
	s_or_b64 vcc, s[2:3], s[6:7]
	v_cndmask_b32_e32 v0, v0, v1, vcc
	v_ashrrev_i32_e32 v1, 31, v0
	v_lshlrev_b64 v[0:1], 6, v[0:1]
	v_lshl_add_u64 v[0:1], v[96:97], 0, v[0:1]
	global_load_dwordx3 v[0:2], v[0:1], off nt
	v_lshlrev_b32_e32 v62, 16, v37
	v_and_b32_e32 v63, 0xffff0000, v37
	v_lshlrev_b32_e32 v64, 16, v36
	v_and_b32_e32 v65, 0xffff0000, v36
	v_lshlrev_b32_e32 v36, 16, v35
	v_and_b32_e32 v37, 0xffff0000, v35
	v_lshlrev_b32_e32 v66, 16, v34
	v_and_b32_e32 v67, 0xffff0000, v34
	v_lshlrev_b32_e32 v70, 16, v28
	v_and_b32_e32 v71, 0xffff0000, v28
	v_add_f32_e32 v3, v63, v62
	v_add_f32_e32 v28, v65, v64
	v_lshlrev_b32_e32 v34, 16, v31
	v_and_b32_e32 v35, 0xffff0000, v31
	v_lshlrev_b32_e32 v68, 16, v30
	v_and_b32_e32 v69, 0xffff0000, v30
	v_lshlrev_b32_e32 v30, 16, v29
	v_and_b32_e32 v31, 0xffff0000, v29
	v_add_f32_e32 v3, v28, v3
	v_add_f32_e32 v28, v37, v36
	v_add_f32_e32 v29, v67, v66
	v_add_f32_e32 v28, v29, v28
	v_add_f32_e32 v3, v28, v3
	v_add_f32_e32 v28, v35, v34
	v_add_f32_e32 v29, v69, v68
	v_add_f32_e32 v28, v29, v28
	v_add_f32_e32 v29, v31, v30
	v_add_f32_e32 v39, v71, v70
	v_add_f32_e32 v29, v39, v29
	v_add_f32_e32 v28, v29, v28
	v_add_f32_e32 v3, v28, v3
	s_mov_b32 s11, 0xf800000
	v_cvt_pk_f32_fp8_sdwa v[178:179], v60 src0_sel:WORD_1
	v_add_f32_dpp v3, v3, v3 quad_perm:[1,0,3,2] row_mask:0xf bank_mask:0xf bound_ctrl:1
	v_cvt_pk_f32_fp8_e32 v[180:181], v61
	v_cvt_pk_f32_fp8_e32 v[182:183], v58
	v_add_f32_dpp v3, v3, v3 quad_perm:[2,3,0,1] row_mask:0xf bank_mask:0xf bound_ctrl:1
	v_cvt_pk_f32_fp8_sdwa v[184:185], v58 src0_sel:WORD_1
	v_cvt_pk_f32_fp8_e32 v[186:187], v59
	v_add_f32_dpp v3, v3, v3 row_half_mirror row_mask:0xf bank_mask:0xf bound_ctrl:1
	v_cvt_pk_f32_fp8_sdwa v[58:59], v59 src0_sel:WORD_1
	v_cvt_pk_f32_fp8_e32 v[188:189], v56
	v_add_f32_dpp v3, v3, v3 row_mirror row_mask:0xf bank_mask:0xf bound_ctrl:1
	ds_swizzle_b32 v28, v3 offset:swizzle(SWAP,16)
	v_cvt_pk_f32_fp8_sdwa v[190:191], v56 src0_sel:WORD_1
	v_cvt_pk_f32_fp8_e32 v[192:193], v57
	v_cvt_pk_f32_fp8_sdwa v[56:57], v57 src0_sel:WORD_1
	v_cvt_pk_f32_fp8_e32 v[194:195], v54
	s_waitcnt lgkmcnt(0)
	v_add_f32_e32 v3, v3, v28
	v_mov_b32_e32 v28, v3
	s_nop 1
	v_permlane32_swap_b32_e32 v3, v28
	v_add_f32_e32 v3, v3, v28
	v_mul_f32_e32 v28, 0x3a800000, v3
	v_pk_add_f32 v[168:169], v[70:71], v[28:29] op_sel_hi:[1,0] neg_lo:[0,1] neg_hi:[0,1]
	v_pk_add_f32 v[30:31], v[30:31], v[28:29] op_sel_hi:[1,0] neg_lo:[0,1] neg_hi:[0,1]
	v_pk_add_f32 v[170:171], v[68:69], v[28:29] op_sel_hi:[1,0] neg_lo:[0,1] neg_hi:[0,1]
	v_pk_add_f32 v[34:35], v[34:35], v[28:29] op_sel_hi:[1,0] neg_lo:[0,1] neg_hi:[0,1]
	v_pk_add_f32 v[172:173], v[66:67], v[28:29] op_sel_hi:[1,0] neg_lo:[0,1] neg_hi:[0,1]
	v_pk_add_f32 v[36:37], v[36:37], v[28:29] op_sel_hi:[1,0] neg_lo:[0,1] neg_hi:[0,1]
	v_pk_add_f32 v[174:175], v[64:65], v[28:29] op_sel_hi:[1,0] neg_lo:[0,1] neg_hi:[0,1]
	v_pk_add_f32 v[28:29], v[62:63], v[28:29] op_sel_hi:[1,0] neg_lo:[0,1] neg_hi:[0,1]
	v_pk_mul_f32 v[74:75], v[174:175], v[174:175]
	v_pk_mul_f32 v[76:77], v[28:29], v[28:29]
	v_pk_mul_f32 v[70:71], v[172:173], v[172:173]
	v_pk_mul_f32 v[72:73], v[36:37], v[36:37]
	v_add_f32_e32 v3, v76, v77
	v_add_f32_e32 v39, v74, v75
	v_add_f32_e32 v3, v39, v3
	v_add_f32_e32 v39, v72, v73
	v_add_f32_e32 v41, v70, v71
	v_pk_mul_f32 v[66:67], v[170:171], v[170:171]
	v_pk_mul_f32 v[68:69], v[34:35], v[34:35]
	v_add_f32_e32 v39, v41, v39
	v_pk_mul_f32 v[62:63], v[168:169], v[168:169]
	v_pk_mul_f32 v[64:65], v[30:31], v[30:31]
	v_add_f32_e32 v3, v39, v3
	v_add_f32_e32 v39, v68, v69
	v_add_f32_e32 v41, v66, v67
	v_add_f32_e32 v39, v41, v39
	v_add_f32_e32 v41, v64, v65
	v_add_f32_e32 v43, v62, v63
	ds_read_b128 v[62:65], v225
	ds_read_b128 v[82:85], v225 offset:1024
	ds_read_b128 v[86:89], v225 offset:2048
	ds_read_b128 v[90:93], v225 offset:3072
	ds_read_b128 v[66:69], v225 offset:4096
	ds_read_b128 v[70:73], v225 offset:5120
	ds_read_b128 v[74:77], v225 offset:6144
	ds_read_b128 v[78:81], v225 offset:7168
	v_add_f32_e32 v41, v43, v41
	v_add_f32_e32 v39, v41, v39
	v_add_f32_e32 v3, v39, v3
	v_cvt_pk_f32_fp8_sdwa v[196:197], v54 src0_sel:WORD_1
	v_cvt_pk_f32_fp8_e32 v[198:199], v55
	v_add_f32_dpp v3, v3, v3 quad_perm:[1,0,3,2] row_mask:0xf bank_mask:0xf bound_ctrl:1
	v_cvt_pk_f32_fp8_sdwa v[54:55], v55 src0_sel:WORD_1
	v_cvt_pk_f32_fp8_e32 v[200:201], v52
	v_add_f32_dpp v3, v3, v3 quad_perm:[2,3,0,1] row_mask:0xf bank_mask:0xf bound_ctrl:1
	v_cvt_pk_f32_fp8_sdwa v[204:205], v52 src0_sel:WORD_1
	v_cvt_pk_f32_fp8_e32 v[206:207], v53
	v_add_f32_dpp v3, v3, v3 row_half_mirror row_mask:0xf bank_mask:0xf bound_ctrl:1
	v_cvt_pk_f32_fp8_sdwa v[52:53], v53 src0_sel:WORD_1
	v_cvt_pk_f32_fp8_e32 v[208:209], v50
	v_add_f32_dpp v3, v3, v3 row_mirror row_mask:0xf bank_mask:0xf bound_ctrl:1
	ds_swizzle_b32 v39, v3 offset:swizzle(SWAP,16)
	v_cvt_pk_f32_fp8_sdwa v[210:211], v50 src0_sel:WORD_1
	v_cvt_pk_f32_fp8_e32 v[212:213], v51
	v_cvt_pk_f32_fp8_sdwa v[50:51], v51 src0_sel:WORD_1
	v_cvt_pk_f32_fp8_e32 v[214:215], v48
	s_waitcnt lgkmcnt(0)
; __device__ __forceinline__ float wave_sum(float v) { v += dpp_f<0xB1>(v); v += dpp_f<0x4E>(v); v += dpp_f<0x141>(v); v += dpp_f<0x140>(v); v += xor_sw<16>(v); return sum_x32(v); }
; __device__ __forceinline__ void ln_row16(float (&v)[16], const float* lng, const float* lnb, int lane, float (&o)[16]) {
;     ...
;     const float rstd = 1.0f / sqrtf(wave_sum(s2) * (1.0f / D) + LN_EPS);
; #pragma unroll
;     for (int hf = 0; hf < 2; ++hf) { const int col = 512 * hf + 8 * lane;
;         const f32x4 g0 = *(const f32x4*)(lng + col), g1 = *(const f32x4*)(lng + col + 4), b0 = *(const f32x4*)(lnb + col), b1 = *(const f32x4*)(lnb + col + 4);
; #pragma unroll
;         for (int i = 0; i < 4; ++i) { o[8 * hf + i] = v[8 * hf + i] * rstd * g0[i] + b0[i]; o[8 * hf + 4 + i] = v[8 * hf + 4 + i] * rstd * g1[i] + b1[i]; } }
; __global__ void __launch_bounds__(NWAVES * 64, 2) mk_fwd(Args args) {
;     ...
;                     ln_row16(v, lng1, lnb1, lane, x1);
; #pragma unroll
;                     for (int hf = 0; hf < 2; ++hf) { float f[8];
; #pragma unroll
;                         for (int i = 0; i < 8; ++i) v[8 * hf + i] = ALPHA * x1[8 * hf + i];
; #pragma unroll
;                         for (int k = 0; k < 4; ++k) { unpack8_f8(yr[j][k][hf], f);
; #pragma unroll
;                             for (int i = 0; i < 8; ++i) v[8 * hf + i] += gt[j][k] * f[i]; } }
;                     ln_row16(v, lng, lnb, lane, o[j]);
	v_add_f32_e32 v3, v3, v39
	v_mov_b32_e32 v39, v3
	s_nop 1
	v_permlane32_swap_b32_e32 v3, v39
	v_add_f32_e32 v3, v3, v39
	v_fmamk_f32 v3, v3, 0x3a800000, v250
	v_mul_f32_e32 v39, 0x4f800000, v3
	v_cmp_gt_f32_e32 vcc, s11, v3
	v_cvt_pk_f32_fp8_sdwa v[216:217], v48 src0_sel:WORD_1
	v_cvt_pk_f32_fp8_e32 v[218:219], v49
	v_cndmask_b32_e32 v3, v3, v39, vcc
	v_sqrt_f32_e32 v39, v3
	v_cvt_pk_f32_fp8_sdwa v[48:49], v49 src0_sel:WORD_1
	v_cvt_pk_f32_fp8_e32 v[226:227], v46
	v_cvt_pk_f32_fp8_sdwa v[228:229], v46 src0_sel:WORD_1
	v_add_u32_e32 v41, -1, v39
	v_fma_f32 v43, -v41, v39, v3
	v_cmp_ge_f32_e64 s[6:7], 0, v43
	v_add_u32_e32 v43, 1, v39
	v_cvt_pk_f32_fp8_e32 v[230:231], v47
	v_cndmask_b32_e64 v41, v39, v41, s[6:7]
	v_fma_f32 v39, -v43, v39, v3
	v_cmp_lt_f32_e64 s[6:7], 0, v39
	v_cvt_pk_f32_fp8_sdwa v[46:47], v47 src0_sel:WORD_1
	v_cvt_pk_f32_fp8_e32 v[232:233], v156
	v_cndmask_b32_e64 v39, v41, v43, s[6:7]
	v_mul_f32_e32 v41, 0x37800000, v39
	v_cndmask_b32_e32 v39, v39, v41, vcc
	v_cmp_class_f32_e32 vcc, v3, v251
	v_cvt_pk_f32_fp8_e32 v[238:239], v154
	v_cvt_pk_f32_fp8_e32 v[244:245], v152
	v_cndmask_b32_e32 v3, v39, v3, vcc
	v_div_scale_f32 v39, s[6:7], v3, v3, 1.0
	v_rcp_f32_e32 v41, v39
	v_cvt_pk_f32_fp8_sdwa v[234:235], v156 src0_sel:WORD_1
	v_cvt_pk_f32_fp8_sdwa v[240:241], v154 src0_sel:WORD_1
	v_cvt_pk_f32_fp8_sdwa v[246:247], v152 src0_sel:WORD_1
	v_fma_f32 v43, -v39, v41, 1.0
	v_fmac_f32_e32 v41, v43, v41
	v_div_scale_f32 v43, vcc, 1.0, v3, 1.0
	v_mul_f32_e32 v45, v43, v41
	v_fma_f32 v147, -v39, v45, v43
	v_fmac_f32_e32 v45, v147, v41
	v_fma_f32 v39, -v39, v45, v43
	v_div_fmas_f32 v39, v39, v41, v45
	v_div_fixup_f32 v176, v39, v3, 1.0
	v_pk_mul_f32 v[168:169], v[168:169], v[176:177] op_sel_hi:[1,0]
	v_pk_mul_f32 v[170:171], v[170:171], v[176:177] op_sel_hi:[1,0]
	v_pk_mul_f32 v[30:31], v[30:31], v[176:177] op_sel_hi:[1,0]
	v_pk_mul_f32 v[34:35], v[34:35], v[176:177] op_sel_hi:[1,0]
	v_pk_mul_f32 v[172:173], v[172:173], v[176:177] op_sel_hi:[1,0]
	v_pk_mul_f32 v[174:175], v[174:175], v[176:177] op_sel_hi:[1,0]
	v_pk_mul_f32 v[36:37], v[36:37], v[176:177] op_sel_hi:[1,0]
	v_pk_mul_f32 v[28:29], v[28:29], v[176:177] op_sel_hi:[1,0]
	v_cvt_pk_f32_fp8_e32 v[176:177], v60
	v_cvt_pk_f32_fp8_sdwa v[60:61], v61 src0_sel:WORD_1
	s_waitcnt lgkmcnt(0)
	v_pk_fma_f32 v[34:35], v[64:65], v[34:35], v[92:93]
	v_pk_fma_f32 v[168:169], v[82:83], v[168:169], v[86:87]
	v_pk_mul_f32 v[176:177], v[44:45], v[176:177] op_sel_hi:[0,1]
	v_pk_mul_f32 v[60:61], v[44:45], v[60:61] op_sel_hi:[0,1]
	v_pk_fma_f32 v[34:35], v[34:35], s[60:61], v[60:61] op_sel_hi:[1,0,1]
	v_pk_fma_f32 v[168:169], v[168:169], s[60:61], v[176:177] op_sel_hi:[1,0,1]
	v_pk_fma_f32 v[34:35], v[42:43], v[58:59], v[34:35] op_sel_hi:[0,1,1]
	v_pk_fma_f32 v[34:35], v[40:41], v[56:57], v[34:35] op_sel_hi:[0,1,1]
	v_pk_fma_f32 v[34:35], v[38:39], v[54:55], v[34:35] op_sel_hi:[0,1,1]
	s_waitcnt lgkmcnt(0)
	v_pk_fma_f32 v[54:55], v[172:173], v[66:67], v[70:71]
	v_pk_mul_f32 v[56:57], v[44:45], v[200:201] op_sel_hi:[0,1]
	v_pk_fma_f32 v[30:31], v[84:85], v[30:31], v[88:89]
	v_pk_mul_f32 v[176:177], v[44:45], v[178:179] op_sel_hi:[0,1]
	v_pk_fma_f32 v[54:55], v[54:55], s[60:61], v[56:57] op_sel_hi:[1,0,1]
	v_pk_fma_f32 v[36:37], v[36:37], v[68:69], v[72:73]
	v_pk_mul_f32 v[56:57], v[44:45], v[204:205] op_sel_hi:[0,1]
	v_pk_fma_f32 v[30:31], v[30:31], s[60:61], v[176:177] op_sel_hi:[1,0,1]
	v_pk_mul_f32 v[176:177], v[44:45], v[180:181] op_sel_hi:[0,1]
	v_pk_fma_f32 v[36:37], v[36:37], s[60:61], v[56:57] op_sel_hi:[1,0,1]
	s_waitcnt lgkmcnt(0)
	v_pk_fma_f32 v[56:57], v[174:175], v[74:75], v[78:79]
	v_pk_mul_f32 v[58:59], v[44:45], v[206:207] op_sel_hi:[0,1]
	v_pk_fma_f32 v[28:29], v[28:29], v[76:77], v[80:81]
	v_pk_mul_f32 v[44:45], v[44:45], v[52:53] op_sel_hi:[0,1]
	v_pk_fma_f32 v[170:171], v[62:63], v[170:171], v[90:91]
	v_pk_fma_f32 v[56:57], v[56:57], s[60:61], v[58:59] op_sel_hi:[1,0,1]
	v_pk_fma_f32 v[28:29], v[28:29], s[60:61], v[44:45] op_sel_hi:[1,0,1]
	v_pk_fma_f32 v[170:171], v[170:171], s[60:61], v[176:177] op_sel_hi:[1,0,1]
	v_pk_fma_f32 v[56:57], v[42:43], v[212:213], v[56:57] op_sel_hi:[0,1,1]
	v_pk_fma_f32 v[28:29], v[42:43], v[50:51], v[28:29] op_sel_hi:[0,1,1]
	v_pk_fma_f32 v[168:169], v[42:43], v[182:183], v[168:169] op_sel_hi:[0,1,1]
	v_pk_fma_f32 v[30:31], v[42:43], v[184:185], v[30:31] op_sel_hi:[0,1,1]
	v_pk_fma_f32 v[170:171], v[42:43], v[186:187], v[170:171] op_sel_hi:[0,1,1]
	v_pk_fma_f32 v[54:55], v[42:43], v[208:209], v[54:55] op_sel_hi:[0,1,1]
	v_pk_fma_f32 v[36:37], v[42:43], v[210:211], v[36:37] op_sel_hi:[0,1,1]
	v_pk_fma_f32 v[56:57], v[40:41], v[218:219], v[56:57] op_sel_hi:[0,1,1]
	v_pk_fma_f32 v[28:29], v[40:41], v[48:49], v[28:29] op_sel_hi:[0,1,1]
	v_pk_fma_f32 v[168:169], v[40:41], v[188:189], v[168:169] op_sel_hi:[0,1,1]
	v_pk_fma_f32 v[30:31], v[40:41], v[190:191], v[30:31] op_sel_hi:[0,1,1]
	v_pk_fma_f32 v[170:171], v[40:41], v[192:193], v[170:171] op_sel_hi:[0,1,1]
	v_pk_fma_f32 v[54:55], v[40:41], v[214:215], v[54:55] op_sel_hi:[0,1,1]
	v_pk_fma_f32 v[36:37], v[40:41], v[216:217], v[36:37] op_sel_hi:[0,1,1]
	v_pk_fma_f32 v[56:57], v[38:39], v[230:231], v[56:57] op_sel_hi:[0,1,1]
	v_pk_fma_f32 v[28:29], v[38:39], v[46:47], v[28:29] op_sel_hi:[0,1,1]
	v_pk_fma_f32 v[168:169], v[38:39], v[194:195], v[168:169] op_sel_hi:[0,1,1]
	v_pk_fma_f32 v[30:31], v[38:39], v[196:197], v[30:31] op_sel_hi:[0,1,1]
	v_pk_fma_f32 v[170:171], v[38:39], v[198:199], v[170:171] op_sel_hi:[0,1,1]
	v_pk_fma_f32 v[54:55], v[38:39], v[226:227], v[54:55] op_sel_hi:[0,1,1]
	v_pk_fma_f32 v[36:37], v[38:39], v[228:229], v[36:37] op_sel_hi:[0,1,1]
	v_add_f32_e32 v3, v28, v29
	v_add_f32_e32 v38, v56, v57
	v_add_f32_e32 v3, v38, v3
	v_add_f32_e32 v38, v36, v37
	v_add_f32_e32 v39, v54, v55
	v_add_f32_e32 v38, v39, v38
	v_add_f32_e32 v3, v38, v3
	v_add_f32_e32 v38, v34, v35
	v_add_f32_e32 v39, v170, v171
	v_add_f32_e32 v38, v39, v38
	v_add_f32_e32 v39, v30, v31
	v_add_f32_e32 v40, v168, v169
	v_add_f32_e32 v39, v40, v39
	v_add_f32_e32 v38, v39, v38
	v_add_f32_e32 v3, v38, v3
	v_lshlrev_b32_e32 v184, 16, v27
	v_and_b32_e32 v185, 0xffff0000, v27
	v_add_f32_dpp v3, v3, v3 quad_perm:[1,0,3,2] row_mask:0xf bank_mask:0xf bound_ctrl:1
	v_lshlrev_b32_e32 v186, 16, v26
	v_and_b32_e32 v187, 0xffff0000, v26
	v_add_f32_dpp v3, v3, v3 quad_perm:[2,3,0,1] row_mask:0xf bank_mask:0xf bound_ctrl:1
	v_lshlrev_b32_e32 v26, 16, v25
	v_and_b32_e32 v27, 0xffff0000, v25
	v_add_f32_dpp v3, v3, v3 row_half_mirror row_mask:0xf bank_mask:0xf bound_ctrl:1
	v_lshlrev_b32_e32 v188, 16, v24
	v_and_b32_e32 v189, 0xffff0000, v24
	v_add_f32_dpp v3, v3, v3 row_mirror row_mask:0xf bank_mask:0xf bound_ctrl:1
	ds_swizzle_b32 v38, v3 offset:swizzle(SWAP,16)
	v_lshlrev_b32_e32 v24, 16, v23
	v_and_b32_e32 v25, 0xffff0000, v23
	v_lshlrev_b32_e32 v190, 16, v22
	v_and_b32_e32 v191, 0xffff0000, v22
	s_waitcnt lgkmcnt(0)
; __device__ __forceinline__ float wave_sum(float v) { v += dpp_f<0xB1>(v); v += dpp_f<0x4E>(v); v += dpp_f<0x141>(v); v += dpp_f<0x140>(v); v += xor_sw<16>(v); return sum_x32(v); }
; __device__ __forceinline__ void ln_row16(float (&v)[16], const float* lng, const float* lnb, int lane, float (&o)[16]) {
;     const float s = ((v[0] + v[1]) + (v[2] + v[3])) + ((v[4] + v[5]) + (v[6] + v[7])) + (((v[8] + v[9]) + (v[10] + v[11])) + ((v[12] + v[13]) + (v[14] + v[15])));
;     const float mean = wave_sum(s) * (1.0f / D);
; #pragma unroll
;     for (int i = 0; i < 16; ++i) v[i] -= mean;
;     const float s2 = ((v[0] * v[0] + v[1] * v[1]) + (v[2] * v[2] + v[3] * v[3])) + ((v[4] * v[4] + v[5] * v[5]) + (v[6] * v[6] + v[7] * v[7]))
;                    + (((v[8] * v[8] + v[9] * v[9]) + (v[10] * v[10] + v[11] * v[11])) + ((v[12] * v[12] + v[13] * v[13]) + (v[14] * v[14] + v[15] * v[15])));
;     const float rstd = 1.0f / sqrtf(wave_sum(s2) * (1.0f / D) + LN_EPS);
; #pragma unroll
;     for (int hf = 0; hf < 2; ++hf) { const int col = 512 * hf + 8 * lane;
;         const f32x4 g0 = *(const f32x4*)(lng + col), g1 = *(const f32x4*)(lng + col + 4), b0 = *(const f32x4*)(lnb + col), b1 = *(const f32x4*)(lnb + col + 4);
; #pragma unroll
;         for (int i = 0; i < 4; ++i) { o[8 * hf + i] = v[8 * hf + i] * rstd * g0[i] + b0[i]; o[8 * hf + 4 + i] = v[8 * hf + 4 + i] * rstd * g1[i] + b1[i]; } }
; __global__ void __launch_bounds__(NWAVES * 64, 2) mk_fwd(Args args) {
;     ...
;                     ln_row16(v, lng1, lnb1, lane, x1);
; #pragma unroll
;                     for (int hf = 0; hf < 2; ++hf) { float f[8];
; #pragma unroll
;                         for (int i = 0; i < 8; ++i) v[8 * hf + i] = ALPHA * x1[8 * hf + i];
; #pragma unroll
;                         for (int k = 0; k < 4; ++k) { unpack8_f8(yr[j][k][hf], f);
; #pragma unroll
;                             for (int i = 0; i < 8; ++i) v[8 * hf + i] += gt[j][k] * f[i]; } }
;                     ln_row16(v, lng, lnb, lane, o[j]);
	v_add_f32_e32 v3, v3, v38
	v_mov_b32_e32 v38, v3
	s_nop 1
	v_permlane32_swap_b32_e32 v3, v38
	v_add_f32_e32 v3, v3, v38
	v_mul_f32_e32 v38, 0x3a800000, v3
	v_pk_add_f32 v[176:177], v[168:169], v[38:39] op_sel_hi:[1,0] neg_lo:[0,1] neg_hi:[0,1]
	v_pk_add_f32 v[178:179], v[30:31], v[38:39] op_sel_hi:[1,0] neg_lo:[0,1] neg_hi:[0,1]
	v_pk_add_f32 v[180:181], v[170:171], v[38:39] op_sel_hi:[1,0] neg_lo:[0,1] neg_hi:[0,1]
	v_pk_add_f32 v[182:183], v[34:35], v[38:39] op_sel_hi:[1,0] neg_lo:[0,1] neg_hi:[0,1]
	v_pk_add_f32 v[172:173], v[54:55], v[38:39] op_sel_hi:[1,0] neg_lo:[0,1] neg_hi:[0,1]
	v_pk_add_f32 v[168:169], v[36:37], v[38:39] op_sel_hi:[1,0] neg_lo:[0,1] neg_hi:[0,1]
	v_pk_add_f32 v[174:175], v[56:57], v[38:39] op_sel_hi:[1,0] neg_lo:[0,1] neg_hi:[0,1]
	v_pk_add_f32 v[170:171], v[28:29], v[38:39] op_sel_hi:[1,0] neg_lo:[0,1] neg_hi:[0,1]
	v_pk_mul_f32 v[28:29], v[176:177], v[176:177]
	v_pk_mul_f32 v[30:31], v[178:179], v[178:179]
	v_pk_mul_f32 v[34:35], v[180:181], v[180:181]
	v_pk_mul_f32 v[36:37], v[182:183], v[182:183]
	v_pk_mul_f32 v[38:39], v[172:173], v[172:173]
	v_pk_mul_f32 v[40:41], v[168:169], v[168:169]
	v_pk_mul_f32 v[42:43], v[174:175], v[174:175]
	v_pk_mul_f32 v[44:45], v[170:171], v[170:171]
	v_add_f32_e32 v42, v42, v43
	v_add_f32_e32 v3, v44, v45
	v_add_f32_e32 v40, v40, v41
	v_add_f32_e32 v38, v38, v39
	v_add_f32_e32 v36, v36, v37
	v_add_f32_e32 v34, v34, v35
	v_add_f32_e32 v30, v30, v31
	v_add_f32_e32 v28, v28, v29
	v_add_f32_e32 v3, v42, v3
	v_add_f32_e32 v38, v38, v40
	v_add_f32_e32 v34, v34, v36
	v_add_f32_e32 v28, v28, v30
	v_add_f32_e32 v3, v38, v3
	v_add_f32_e32 v28, v28, v34
	v_add_f32_e32 v3, v28, v3
	v_lshlrev_b32_e32 v22, 16, v21
	v_and_b32_e32 v23, 0xffff0000, v21
	v_add_f32_dpp v3, v3, v3 quad_perm:[1,0,3,2] row_mask:0xf bank_mask:0xf bound_ctrl:1
	v_lshlrev_b32_e32 v192, 16, v20
	v_and_b32_e32 v193, 0xffff0000, v20
	v_add_f32_dpp v3, v3, v3 quad_perm:[2,3,0,1] row_mask:0xf bank_mask:0xf bound_ctrl:1
	v_add_f32_e32 v20, v185, v184
	v_add_f32_e32 v21, v187, v186
	v_add_f32_dpp v3, v3, v3 row_half_mirror row_mask:0xf bank_mask:0xf bound_ctrl:1
	v_add_f32_e32 v20, v21, v20
	v_add_f32_e32 v21, v27, v26
	v_add_f32_dpp v3, v3, v3 row_mirror row_mask:0xf bank_mask:0xf bound_ctrl:1
	ds_swizzle_b32 v28, v3 offset:swizzle(SWAP,16)
	v_add_f32_e32 v194, v189, v188
	v_add_f32_e32 v21, v194, v21
	v_add_f32_e32 v20, v21, v20
	v_add_f32_e32 v21, v25, v24
	s_waitcnt lgkmcnt(0)
	v_add_f32_e32 v3, v3, v28
	v_mov_b32_e32 v28, v3
	s_nop 1
	v_permlane32_swap_b32_e32 v3, v28
	v_add_f32_e32 v3, v3, v28
	v_fmamk_f32 v3, v3, 0x3a800000, v250
	v_mul_f32_e32 v28, 0x4f800000, v3
	v_cmp_gt_f32_e32 vcc, s11, v3
	v_add_f32_e32 v194, v191, v190
	v_add_f32_e32 v21, v194, v21
	v_cndmask_b32_e32 v3, v3, v28, vcc
	ds_read_b128 v[28:31], v225 offset:8192
	ds_read_b128 v[38:41], v225 offset:9216
	ds_read_b128 v[34:37], v225 offset:10240
	ds_read_b128 v[42:45], v225 offset:11264
	v_sqrt_f32_e32 v46, v3
	v_add_f32_e32 v194, v23, v22
	v_add_f32_e32 v195, v193, v192
	v_add_f32_e32 v194, v195, v194
	v_add_u32_e32 v47, -1, v46
	v_fma_f32 v48, -v47, v46, v3
	v_cmp_ge_f32_e64 s[6:7], 0, v48
	v_add_u32_e32 v48, 1, v46
	v_add_f32_e32 v21, v194, v21
	v_cndmask_b32_e64 v47, v46, v47, s[6:7]
	v_fma_f32 v46, -v48, v46, v3
	v_add_f32_e32 v20, v21, v20
	v_cmp_lt_f32_e64 s[6:7], 0, v46
	v_cvt_pk_f32_fp8_e32 v[212:213], v163
	v_add_f32_dpp v20, v20, v20 quad_perm:[1,0,3,2] row_mask:0xf bank_mask:0xf bound_ctrl:1
	v_cndmask_b32_e64 v46, v47, v48, s[6:7]
	v_mul_f32_e32 v47, 0x37800000, v46
	v_add_f32_dpp v20, v20, v20 quad_perm:[2,3,0,1] row_mask:0xf bank_mask:0xf bound_ctrl:1
	v_cndmask_b32_e32 v46, v46, v47, vcc
	v_cmp_class_f32_e32 vcc, v3, v251
	v_add_f32_dpp v20, v20, v20 row_half_mirror row_mask:0xf bank_mask:0xf bound_ctrl:1
	v_cvt_pk_f32_fp8_e32 v[218:219], v161
	v_cndmask_b32_e32 v3, v46, v3, vcc
	v_add_f32_dpp v20, v20, v20 row_mirror row_mask:0xf bank_mask:0xf bound_ctrl:1
	ds_swizzle_b32 v21, v20 offset:swizzle(SWAP,16)
	v_div_scale_f32 v147, s[6:7], v3, v3, 1.0
	v_rcp_f32_e32 v149, v147
	ds_read_b128 v[46:49], v225 offset:12288
	ds_read_b128 v[54:57], v225 offset:13312
	ds_read_b128 v[50:53], v225 offset:14336
	ds_read_b128 v[58:61], v225 offset:15360
	s_waitcnt lgkmcnt(0)
; __device__ __forceinline__ void unpack8(const u32x4 w, float (&f)[8]) { f[0] = bf_lo(w.x); f[1] = bf_hi(w.x); f[2] = bf_lo(w.y); f[3] = bf_hi(w.y); f[4] = bf_lo(w.z); f[5] = bf_hi(w.z); f[6] = bf_lo(w.w); f[7] = bf_hi(w.w); }
; __device__ __forceinline__ float wave_sum(float v) { v += dpp_f<0xB1>(v); v += dpp_f<0x4E>(v); v += dpp_f<0x141>(v); v += dpp_f<0x140>(v); v += xor_sw<16>(v); return sum_x32(v); }
; __device__ __forceinline__ void ln_row16(float (&v)[16], const float* lng, const float* lnb, int lane, float (&o)[16]) {
;     ...
;     const float s2 = ((v[0] * v[0] + v[1] * v[1]) + (v[2] * v[2] + v[3] * v[3])) + ((v[4] * v[4] + v[5] * v[5]) + (v[6] * v[6] + v[7] * v[7]))
;                    + (((v[8] * v[8] + v[9] * v[9]) + (v[10] * v[10] + v[11] * v[11])) + ((v[12] * v[12] + v[13] * v[13]) + (v[14] * v[14] + v[15] * v[15])));
;     const float rstd = 1.0f / sqrtf(wave_sum(s2) * (1.0f / D) + LN_EPS);
; #pragma unroll
;     for (int hf = 0; hf < 2; ++hf) { const int col = 512 * hf + 8 * lane;
;         const f32x4 g0 = *(const f32x4*)(lng + col), g1 = *(const f32x4*)(lng + col + 4), b0 = *(const f32x4*)(lnb + col), b1 = *(const f32x4*)(lnb + col + 4);
; #pragma unroll
;         for (int i = 0; i < 4; ++i) { o[8 * hf + i] = v[8 * hf + i] * rstd * g0[i] + b0[i]; o[8 * hf + 4 + i] = v[8 * hf + 4 + i] * rstd * g1[i] + b1[i]; } }
; __global__ void __launch_bounds__(NWAVES * 64, 2) mk_fwd(Args args) {
;     ...
;                 for (int j = 0; j < 2; ++j) {
;                     float v[16], x1[16];
; #pragma unroll
;                     for (int hf = 0; hf < 2; ++hf) { float f[8]; unpack8(xr[j][hf], f);
; #pragma unroll
;                         for (int i = 0; i < 8; ++i) v[8 * hf + i] = f[i]; }
;                     ln_row16(v, lng1, lnb1, lane, x1);
; #pragma unroll
;                     for (int hf = 0; hf < 2; ++hf) { float f[8];
; #pragma unroll
;                         for (int i = 0; i < 8; ++i) v[8 * hf + i] = ALPHA * x1[8 * hf + i];
; #pragma unroll
;                         for (int k = 0; k < 4; ++k) { unpack8_f8(yr[j][k][hf], f);
; #pragma unroll
;                             for (int i = 0; i < 8; ++i) v[8 * hf + i] += gt[j][k] * f[i]; } }
;                     ln_row16(v, lng, lnb, lane, o[j]);
	v_add_f32_e32 v20, v20, v21
	v_mov_b32_e32 v21, v20
	v_fma_f32 v151, -v147, v149, 1.0
	v_fmac_f32_e32 v149, v151, v149
	v_div_scale_f32 v151, vcc, 1.0, v3, 1.0
	v_permlane32_swap_b32_e32 v20, v21
	v_mul_f32_e32 v202, v151, v149
	v_add_f32_e32 v20, v20, v21
	v_fma_f32 v194, -v147, v202, v151
	v_mul_f32_e32 v20, 0x3a800000, v20
	v_fmac_f32_e32 v202, v194, v149
	v_pk_add_f32 v[192:193], v[192:193], v[20:21] op_sel_hi:[1,0] neg_lo:[0,1] neg_hi:[0,1]
	v_pk_add_f32 v[194:195], v[22:23], v[20:21] op_sel_hi:[1,0] neg_lo:[0,1] neg_hi:[0,1]
	v_pk_add_f32 v[190:191], v[190:191], v[20:21] op_sel_hi:[1,0] neg_lo:[0,1] neg_hi:[0,1]
	v_pk_add_f32 v[196:197], v[24:25], v[20:21] op_sel_hi:[1,0] neg_lo:[0,1] neg_hi:[0,1]
	v_pk_add_f32 v[188:189], v[188:189], v[20:21] op_sel_hi:[1,0] neg_lo:[0,1] neg_hi:[0,1]
	v_pk_add_f32 v[198:199], v[26:27], v[20:21] op_sel_hi:[1,0] neg_lo:[0,1] neg_hi:[0,1]
	v_pk_add_f32 v[186:187], v[186:187], v[20:21] op_sel_hi:[1,0] neg_lo:[0,1] neg_hi:[0,1]
	v_pk_add_f32 v[184:185], v[184:185], v[20:21] op_sel_hi:[1,0] neg_lo:[0,1] neg_hi:[0,1]
	v_pk_mul_f32 v[20:21], v[192:193], v[192:193]
	v_pk_mul_f32 v[22:23], v[194:195], v[194:195]
	v_pk_mul_f32 v[24:25], v[190:191], v[190:191]
	v_pk_mul_f32 v[26:27], v[196:197], v[196:197]
	v_pk_mul_f32 v[200:201], v[188:189], v[188:189]
	v_pk_mul_f32 v[204:205], v[198:199], v[198:199]
	v_pk_mul_f32 v[206:207], v[186:187], v[186:187]
	v_pk_mul_f32 v[208:209], v[184:185], v[184:185]
	v_fma_f32 v147, -v147, v202, v151
	v_add_f32_e32 v151, v208, v209
	v_add_f32_e32 v206, v206, v207
	v_add_f32_e32 v204, v204, v205
	v_add_f32_e32 v200, v200, v201
	v_add_f32_e32 v26, v26, v27
	v_add_f32_e32 v24, v24, v25
	v_add_f32_e32 v22, v22, v23
	v_add_f32_e32 v20, v20, v21
	v_add_f32_e32 v151, v206, v151
	v_add_f32_e32 v200, v200, v204
	v_add_f32_e32 v24, v24, v26
	v_add_f32_e32 v20, v20, v22
	v_add_f32_e32 v151, v200, v151
	v_add_f32_e32 v20, v20, v24
	v_add_f32_e32 v20, v20, v151
	v_cvt_pk_f32_fp8_e32 v[206:207], v165
	v_cvt_pk_f32_fp8_sdwa v[204:205], v164 src0_sel:WORD_1
	v_add_f32_dpp v20, v20, v20 quad_perm:[1,0,3,2] row_mask:0xf bank_mask:0xf bound_ctrl:1
	v_cvt_pk_f32_fp8_e32 v[208:209], v162
	v_cvt_pk_f32_fp8_sdwa v[210:211], v162 src0_sel:WORD_1
	v_add_f32_dpp v20, v20, v20 quad_perm:[2,3,0,1] row_mask:0xf bank_mask:0xf bound_ctrl:1
	v_cvt_pk_f32_fp8_sdwa v[162:163], v163 src0_sel:WORD_1
	v_cvt_pk_f32_fp8_e32 v[214:215], v160
	v_add_f32_dpp v20, v20, v20 row_half_mirror row_mask:0xf bank_mask:0xf bound_ctrl:1
	v_cvt_pk_f32_fp8_sdwa v[216:217], v160 src0_sel:WORD_1
	v_cvt_pk_f32_fp8_sdwa v[160:161], v161 src0_sel:WORD_1
	v_add_f32_dpp v24, v20, v20 row_mirror row_mask:0xf bank_mask:0xf bound_ctrl:1
	ds_swizzle_b32 v25, v24 offset:swizzle(SWAP,16)
	v_div_fmas_f32 v20, v147, v149, v202
	v_div_fixup_f32 v200, v20, v3, 1.0
	v_pk_mul_f32 v[20:21], v[176:177], v[200:201] op_sel_hi:[1,0]
	v_pk_mul_f32 v[22:23], v[180:181], v[200:201] op_sel_hi:[1,0]
	s_waitcnt lgkmcnt(0)
	v_add_f32_e32 v3, v24, v25
	v_mov_b32_e32 v24, v3
	s_nop 1
	v_permlane32_swap_b32_e32 v3, v24
	v_add_f32_e32 v3, v3, v24
	v_fmamk_f32 v3, v3, 0x3a800000, v250
	v_mul_f32_e32 v24, 0x4f800000, v3
	v_cmp_gt_f32_e32 vcc, s11, v3
	v_pk_mul_f32 v[176:177], v[182:183], v[200:201] op_sel_hi:[1,0]
	v_cvt_pk_f32_fp8_e32 v[226:227], v158
	v_cndmask_b32_e32 v3, v3, v24, vcc
	v_sqrt_f32_e32 v26, v3
	s_waitcnt lgkmcnt(0)
	v_pk_fma_f32 v[24:25], v[38:39], v[20:21], v[42:43]
	v_pk_fma_f32 v[20:21], v[28:29], v[22:23], v[34:35]
	v_pk_mul_f32 v[22:23], v[178:179], v[200:201] op_sel_hi:[1,0]
	v_add_u32_e32 v27, -1, v26
	v_fma_f32 v147, -v27, v26, v3
	v_cmp_ge_f32_e64 s[6:7], 0, v147
	v_add_u32_e32 v147, 1, v26
	v_cvt_pk_f32_fp8_sdwa v[228:229], v158 src0_sel:WORD_1
	v_cndmask_b32_e64 v27, v26, v27, s[6:7]
	v_fma_f32 v26, -v147, v26, v3
	v_cmp_lt_f32_e64 s[6:7], 0, v26
	v_cvt_pk_f32_fp8_e32 v[230:231], v159
	v_cvt_pk_f32_fp8_e32 v[236:237], v157
	v_cndmask_b32_e64 v26, v27, v147, s[6:7]
	v_mul_f32_e32 v27, 0x37800000, v26
	v_cndmask_b32_e32 v26, v26, v27, vcc
	v_cmp_class_f32_e32 vcc, v3, v251
	v_cvt_pk_f32_fp8_e32 v[242:243], v155
	v_cvt_pk_f32_fp8_sdwa v[158:159], v159 src0_sel:WORD_1
	v_cndmask_b32_e32 v3, v26, v3, vcc
	v_div_scale_f32 v147, s[6:7], v3, v3, 1.0
	v_rcp_f32_e32 v149, v147
	v_pk_fma_f32 v[26:27], v[40:41], v[22:23], v[44:45]
	v_pk_fma_f32 v[22:23], v[30:31], v[176:177], v[36:37]
	v_cvt_pk_f32_fp8_e32 v[248:249], v153
	v_fma_f32 v151, -v147, v149, 1.0
	v_fmac_f32_e32 v149, v151, v149
	v_div_scale_f32 v151, vcc, 1.0, v3, 1.0
	v_mul_f32_e32 v176, v151, v149
	v_fma_f32 v177, -v147, v176, v151
	v_fmac_f32_e32 v176, v177, v149
	v_fma_f32 v147, -v147, v176, v151
	v_div_fmas_f32 v147, v147, v149, v176
	v_div_fixup_f32 v176, v147, v3, 1.0
	v_pk_mul_f32 v[178:179], v[192:193], v[176:177] op_sel_hi:[1,0]
	v_pk_mul_f32 v[180:181], v[190:191], v[176:177] op_sel_hi:[1,0]
	v_pk_mul_f32 v[182:183], v[194:195], v[176:177] op_sel_hi:[1,0]
	v_pk_mul_f32 v[190:191], v[196:197], v[176:177] op_sel_hi:[1,0]
	v_pk_mul_f32 v[188:189], v[188:189], v[176:177] op_sel_hi:[1,0]
	v_pk_mul_f32 v[186:187], v[186:187], v[176:177] op_sel_hi:[1,0]
	v_pk_mul_f32 v[192:193], v[198:199], v[176:177] op_sel_hi:[1,0]
	v_pk_mul_f32 v[176:177], v[184:185], v[176:177] op_sel_hi:[1,0]
	v_cvt_pk_f32_fp8_e32 v[184:185], v166
	v_cvt_pk_f32_fp8_sdwa v[194:195], v166 src0_sel:WORD_1
	v_cvt_pk_f32_fp8_e32 v[196:197], v167
	v_pk_fma_f32 v[82:83], v[82:83], v[178:179], v[86:87]
	v_pk_mul_f32 v[86:87], v[150:151], v[184:185] op_sel_hi:[0,1]
	v_pk_fma_f32 v[82:83], v[82:83], s[60:61], v[86:87] op_sel_hi:[1,0,1]
	v_pk_fma_f32 v[84:85], v[84:85], v[182:183], v[88:89]
; __device__ __forceinline__ float wave_sum(float v) { v += dpp_f<0xB1>(v); v += dpp_f<0x4E>(v); v += dpp_f<0x141>(v); v += dpp_f<0x140>(v); v += xor_sw<16>(v); return sum_x32(v); }
; __device__ __forceinline__ void ln_row16(float (&v)[16], const float* lng, const float* lnb, int lane, float (&o)[16]) {
;     const float s = ((v[0] + v[1]) + (v[2] + v[3])) + ((v[4] + v[5]) + (v[6] + v[7])) + (((v[8] + v[9]) + (v[10] + v[11])) + ((v[12] + v[13]) + (v[14] + v[15])));
;     const float mean = wave_sum(s) * (1.0f / D);
; #pragma unroll
;     for (int i = 0; i < 16; ++i) v[i] -= mean;
;     const float s2 = ((v[0] * v[0] + v[1] * v[1]) + (v[2] * v[2] + v[3] * v[3])) + ((v[4] * v[4] + v[5] * v[5]) + (v[6] * v[6] + v[7] * v[7]))
;                    + (((v[8] * v[8] + v[9] * v[9]) + (v[10] * v[10] + v[11] * v[11])) + ((v[12] * v[12] + v[13] * v[13]) + (v[14] * v[14] + v[15] * v[15])));
;     const float rstd = 1.0f / sqrtf(wave_sum(s2) * (1.0f / D) + LN_EPS);
; #pragma unroll
;     for (int hf = 0; hf < 2; ++hf) { const int col = 512 * hf + 8 * lane;
;         const f32x4 g0 = *(const f32x4*)(lng + col), g1 = *(const f32x4*)(lng + col + 4), b0 = *(const f32x4*)(lnb + col), b1 = *(const f32x4*)(lnb + col + 4);
; #pragma unroll
;         for (int i = 0; i < 4; ++i) { o[8 * hf + i] = v[8 * hf + i] * rstd * g0[i] + b0[i]; o[8 * hf + 4 + i] = v[8 * hf + 4 + i] * rstd * g1[i] + b1[i]; } }
; __global__ void __launch_bounds__(NWAVES * 64, 2) mk_fwd(Args args) {
;     ...
;                     ln_row16(v, lng1, lnb1, lane, x1);
; #pragma unroll
;                     for (int hf = 0; hf < 2; ++hf) { float f[8];
; #pragma unroll
;                         for (int i = 0; i < 8; ++i) v[8 * hf + i] = ALPHA * x1[8 * hf + i];
; #pragma unroll
;                         for (int k = 0; k < 4; ++k) { unpack8_f8(yr[j][k][hf], f);
; #pragma unroll
;                             for (int i = 0; i < 8; ++i) v[8 * hf + i] += gt[j][k] * f[i]; } }
;                     ln_row16(v, lng, lnb, lane, o[j]);
;                 }
; #pragma unroll
;                 for (int j = 0; j < 2; ++j) {
;                     const int t = tt[j];
;                     if (layer == DEPTH - 1) {
	v_pk_mul_f32 v[86:87], v[150:151], v[194:195] op_sel_hi:[0,1]
	v_cvt_pk_f32_fp8_sdwa v[166:167], v167 src0_sel:WORD_1
	v_pk_fma_f32 v[84:85], v[84:85], s[60:61], v[86:87] op_sel_hi:[1,0,1]
	v_pk_fma_f32 v[62:63], v[62:63], v[180:181], v[90:91]
	v_pk_mul_f32 v[86:87], v[150:151], v[196:197] op_sel_hi:[0,1]
	v_pk_fma_f32 v[62:63], v[62:63], s[60:61], v[86:87] op_sel_hi:[1,0,1]
	v_cvt_pk_f32_fp8_e32 v[198:199], v164
	v_cvt_pk_f32_fp8_sdwa v[164:165], v165 src0_sel:WORD_1
	v_pk_fma_f32 v[62:63], v[148:149], v[206:207], v[62:63] op_sel_hi:[0,1,1]
	v_pk_fma_f32 v[62:63], v[146:147], v[212:213], v[62:63] op_sel_hi:[0,1,1]
	v_pk_fma_f32 v[86:87], v[32:33], v[218:219], v[62:63] op_sel_hi:[0,1,1]
	v_pk_fma_f32 v[62:63], v[64:65], v[190:191], v[92:93]
	v_pk_mul_f32 v[64:65], v[150:151], v[166:167] op_sel_hi:[0,1]
	v_pk_fma_f32 v[62:63], v[62:63], s[60:61], v[64:65] op_sel_hi:[1,0,1]
	v_cvt_pk_f32_fp8_sdwa v[156:157], v157 src0_sel:WORD_1
	v_pk_fma_f32 v[62:63], v[148:149], v[164:165], v[62:63] op_sel_hi:[0,1,1]
	v_pk_fma_f32 v[62:63], v[146:147], v[162:163], v[62:63] op_sel_hi:[0,1,1]
	v_pk_fma_f32 v[64:65], v[32:33], v[160:161], v[62:63] op_sel_hi:[0,1,1]
	v_pk_fma_f32 v[62:63], v[188:189], v[66:67], v[70:71]
	v_pk_mul_f32 v[66:67], v[150:151], v[226:227] op_sel_hi:[0,1]
	v_pk_fma_f32 v[62:63], v[62:63], s[60:61], v[66:67] op_sel_hi:[1,0,1]
	v_pk_mul_f32 v[66:67], v[150:151], v[228:229] op_sel_hi:[0,1]
	v_pk_fma_f32 v[62:63], v[148:149], v[232:233], v[62:63] op_sel_hi:[0,1,1]
	v_pk_fma_f32 v[62:63], v[146:147], v[238:239], v[62:63] op_sel_hi:[0,1,1]
	v_pk_fma_f32 v[70:71], v[32:33], v[244:245], v[62:63] op_sel_hi:[0,1,1]
	v_pk_fma_f32 v[62:63], v[192:193], v[68:69], v[72:73]
	v_cvt_pk_f32_fp8_sdwa v[154:155], v155 src0_sel:WORD_1
	v_pk_fma_f32 v[62:63], v[62:63], s[60:61], v[66:67] op_sel_hi:[1,0,1]
	v_pk_mul_f32 v[66:67], v[150:151], v[230:231] op_sel_hi:[0,1]
	v_pk_fma_f32 v[62:63], v[148:149], v[234:235], v[62:63] op_sel_hi:[0,1,1]
	v_pk_fma_f32 v[62:63], v[146:147], v[240:241], v[62:63] op_sel_hi:[0,1,1]
	v_pk_fma_f32 v[68:69], v[32:33], v[246:247], v[62:63] op_sel_hi:[0,1,1]
	v_pk_fma_f32 v[62:63], v[186:187], v[74:75], v[78:79]
	v_cvt_pk_f32_fp8_sdwa v[152:153], v153 src0_sel:WORD_1
	v_pk_fma_f32 v[62:63], v[62:63], s[60:61], v[66:67] op_sel_hi:[1,0,1]
	v_pk_mul_f32 v[66:67], v[150:151], v[158:159] op_sel_hi:[0,1]
	v_pk_fma_f32 v[62:63], v[148:149], v[236:237], v[62:63] op_sel_hi:[0,1,1]
	v_pk_fma_f32 v[62:63], v[146:147], v[242:243], v[62:63] op_sel_hi:[0,1,1]
	v_pk_fma_f32 v[72:73], v[32:33], v[248:249], v[62:63] op_sel_hi:[0,1,1]
	v_pk_fma_f32 v[62:63], v[176:177], v[76:77], v[80:81]
	v_pk_fma_f32 v[82:83], v[148:149], v[198:199], v[82:83] op_sel_hi:[0,1,1]
	v_pk_fma_f32 v[62:63], v[62:63], s[60:61], v[66:67] op_sel_hi:[1,0,1]
	v_pk_fma_f32 v[84:85], v[148:149], v[204:205], v[84:85] op_sel_hi:[0,1,1]
	v_pk_fma_f32 v[62:63], v[148:149], v[156:157], v[62:63] op_sel_hi:[0,1,1]
	v_pk_fma_f32 v[62:63], v[146:147], v[154:155], v[62:63] op_sel_hi:[0,1,1]
	v_pk_fma_f32 v[82:83], v[146:147], v[208:209], v[82:83] op_sel_hi:[0,1,1]
	v_pk_fma_f32 v[84:85], v[146:147], v[210:211], v[84:85] op_sel_hi:[0,1,1]
	v_pk_fma_f32 v[88:89], v[32:33], v[152:153], v[62:63] op_sel_hi:[0,1,1]
	v_pk_fma_f32 v[82:83], v[32:33], v[214:215], v[82:83] op_sel_hi:[0,1,1]
	v_pk_fma_f32 v[84:85], v[32:33], v[216:217], v[84:85] op_sel_hi:[0,1,1]
	v_add_f32_e32 v3, v88, v89
	v_add_f32_e32 v32, v72, v73
	v_add_f32_e32 v3, v32, v3
	v_add_f32_e32 v32, v68, v69
	v_add_f32_e32 v62, v70, v71
	v_add_f32_e32 v32, v62, v32
	v_add_f32_e32 v3, v32, v3
	v_add_f32_e32 v32, v64, v65
	v_add_f32_e32 v62, v86, v87
	v_add_f32_e32 v32, v62, v32
	v_add_f32_e32 v62, v84, v85
	v_add_f32_e32 v63, v82, v83
	v_add_f32_e32 v62, v63, v62
	v_add_f32_e32 v32, v62, v32
	v_add_f32_e32 v3, v32, v3
	v_pk_mul_f32 v[62:63], v[172:173], v[200:201] op_sel_hi:[1,0]
	v_pk_mul_f32 v[74:75], v[174:175], v[200:201] op_sel_hi:[1,0]
	v_add_f32_dpp v3, v3, v3 quad_perm:[1,0,3,2] row_mask:0xf bank_mask:0xf bound_ctrl:1
	s_waitcnt lgkmcnt(0)
	v_pk_fma_f32 v[66:67], v[62:63], v[54:55], v[58:59]
	v_pk_fma_f32 v[62:63], v[74:75], v[46:47], v[50:51]
	v_add_f32_dpp v3, v3, v3 quad_perm:[2,3,0,1] row_mask:0xf bank_mask:0xf bound_ctrl:1
	s_mov_b64 s[6:7], -1
	s_and_b64 vcc, exec, s[8:9]
	v_add_f32_dpp v3, v3, v3 row_half_mirror row_mask:0xf bank_mask:0xf bound_ctrl:1
	s_nop 1
	v_add_f32_dpp v3, v3, v3 row_mirror row_mask:0xf bank_mask:0xf bound_ctrl:1
	ds_swizzle_b32 v32, v3 offset:swizzle(SWAP,16)
	s_waitcnt lgkmcnt(0)
	v_add_f32_e32 v3, v3, v32
	v_mov_b32_e32 v32, v3
	s_nop 1
	v_permlane32_swap_b32_e32 v3, v32
	v_add_f32_e32 v3, v3, v32
	v_mul_f32_e32 v32, 0x3a800000, v3
	v_pk_add_f32 v[76:77], v[72:73], v[32:33] op_sel_hi:[1,0] neg_lo:[0,1] neg_hi:[0,1]
	v_pk_add_f32 v[72:73], v[88:89], v[32:33] op_sel_hi:[1,0] neg_lo:[0,1] neg_hi:[0,1]
	v_pk_add_f32 v[74:75], v[70:71], v[32:33] op_sel_hi:[1,0] neg_lo:[0,1] neg_hi:[0,1]
	v_pk_add_f32 v[70:71], v[68:69], v[32:33] op_sel_hi:[1,0] neg_lo:[0,1] neg_hi:[0,1]
	v_pk_mul_f32 v[146:147], v[76:77], v[76:77]
	v_pk_mul_f32 v[148:149], v[72:73], v[72:73]
	v_pk_add_f32 v[82:83], v[82:83], v[32:33] op_sel_hi:[1,0] neg_lo:[0,1] neg_hi:[0,1]
	v_pk_add_f32 v[78:79], v[84:85], v[32:33] op_sel_hi:[1,0] neg_lo:[0,1] neg_hi:[0,1]
	v_pk_add_f32 v[84:85], v[86:87], v[32:33] op_sel_hi:[1,0] neg_lo:[0,1] neg_hi:[0,1]
	v_pk_add_f32 v[80:81], v[64:65], v[32:33] op_sel_hi:[1,0] neg_lo:[0,1] neg_hi:[0,1]
	v_pk_mul_f32 v[90:91], v[74:75], v[74:75]
	v_pk_mul_f32 v[92:93], v[70:71], v[70:71]
	v_add_f32_e32 v3, v148, v149
	v_add_f32_e32 v32, v146, v147
	v_add_f32_e32 v3, v32, v3
	v_add_f32_e32 v32, v92, v93
	v_add_f32_e32 v90, v90, v91
	v_pk_mul_f32 v[64:65], v[82:83], v[82:83]
	v_pk_mul_f32 v[68:69], v[78:79], v[78:79]
	v_pk_mul_f32 v[86:87], v[84:85], v[84:85]
	v_pk_mul_f32 v[88:89], v[80:81], v[80:81]
	v_add_f32_e32 v32, v90, v32
	v_add_f32_e32 v3, v32, v3
	v_add_f32_e32 v32, v88, v89
	v_add_f32_e32 v86, v86, v87
	v_add_f32_e32 v68, v68, v69
	v_add_f32_e32 v64, v64, v65
	v_add_f32_e32 v32, v86, v32
	v_add_f32_e32 v64, v64, v68
	v_add_f32_e32 v32, v64, v32
	v_add_f32_e32 v3, v32, v3
	v_pk_mul_f32 v[64:65], v[168:169], v[200:201] op_sel_hi:[1,0]
	v_pk_mul_f32 v[86:87], v[170:171], v[200:201] op_sel_hi:[1,0]
	v_add_f32_dpp v3, v3, v3 quad_perm:[1,0,3,2] row_mask:0xf bank_mask:0xf bound_ctrl:1
	v_pk_fma_f32 v[68:69], v[64:65], v[56:57], v[60:61]
	v_pk_fma_f32 v[64:65], v[86:87], v[48:49], v[52:53]
	v_add_f32_dpp v3, v3, v3 quad_perm:[2,3,0,1] row_mask:0xf bank_mask:0xf bound_ctrl:1
	s_nop 1
	v_add_f32_dpp v3, v3, v3 row_half_mirror row_mask:0xf bank_mask:0xf bound_ctrl:1
	s_nop 1
	v_add_f32_dpp v3, v3, v3 row_mirror row_mask:0xf bank_mask:0xf bound_ctrl:1
	ds_swizzle_b32 v32, v3 offset:swizzle(SWAP,16)
	s_waitcnt lgkmcnt(0)
	v_add_f32_e32 v3, v3, v32
	v_mov_b32_e32 v32, v3
	s_nop 1
	v_permlane32_swap_b32_e32 v3, v32
	s_cbranch_vccz .LBB0_711
; __device__ __forceinline__ u32x4 pack8(const float (&f)[8]) { u32x4 o; o.x = cvt_pk_bf16(f[0], f[1]); o.y = cvt_pk_bf16(f[2], f[3]); o.z = cvt_pk_bf16(f[4], f[5]); o.w = cvt_pk_bf16(f[6], f[7]); return o; }
; __device__ __forceinline__ float wave_max(float v) { v = fmaxf(v, dpp_f<0xB1>(v)); v = fmaxf(v, dpp_f<0x4E>(v)); v = fmaxf(v, dpp_f<0x141>(v)); v = fmaxf(v, dpp_f<0x140>(v)); v = fmaxf(v, xor_sw<16>(v)); return max_x32(v); }
; __device__ __forceinline__ float q8_row16(const float (&o)[16], unsigned char* qrow, int lane) {
;     float am = 0.f;
; #pragma unroll
;     for (int i = 0; i < 16; ++i) am = fmaxf(am, fabsf(o[i]));
;     am = wave_max(am);
;     const float qs = am > 0.f ? am * (1.0f / 127.0f) : 1.0f, qinv = 1.0f / qs;
; #pragma unroll
;     for (int hf = 0; hf < 2; ++hf) { u32x2 q; q.x = q8x4(o[8 * hf], o[8 * hf + 1], o[8 * hf + 2], o[8 * hf + 3], qinv); q.y = q8x4(o[8 * hf + 4], o[8 * hf + 5], o[8 * hf + 6], o[8 * hf + 7], qinv);
;         *(u32x2*)(qrow + 512 * hf + 8 * lane) = q; }
;     return qs;
; }
; __device__ __forceinline__ void store_bf16_row16(const float (&o)[16], bf16_t* row, int lane) {
; #pragma unroll
;     for (int hf = 0; hf < 2; ++hf) { const float (&oh)[8] = *(const float (*)[8])(o + 8 * hf); *(u32x4*)(row + 512 * hf + 8 * lane) = pack8(oh); }
; __global__ void __launch_bounds__(NWAVES * 64, 2) mk_fwd(Args args) {
;     ...
;                     } else {
;                         store_bf16_row16(o[j], XBo + (size_t)t * D, lane);
;                         const float qs = q8_row16(o[j], XQo + (size_t)t * D, lane);
;                         if (lane == 0) SXo[t] = qs;
	v_max3_f32 v89, |v24|, 0, |v25|
	v_max3_f32 v89, v89, |v26|, |v27|
	v_max3_f32 v89, v89, |v20|, |v21|
	v_max3_f32 v89, v89, |v22|, |v23|
	v_max3_f32 v89, v89, |v66|, |v67|
	v_max3_f32 v89, v89, |v68|, |v69|
	v_max3_f32 v89, v89, |v62|, |v63|
	v_max3_f32 v89, v89, |v64|, |v65|
	s_ashr_i32 s11, s10, 31
	s_lshl_b64 s[12:13], s[10:11], 11
	v_mov_b32_dpp v90, v89 quad_perm:[1,0,3,2] row_mask:0xf bank_mask:0xf bound_ctrl:1
	v_max_f32_e32 v90, v90, v90
	v_max_f32_e32 v89, v89, v90
	v_lshl_add_u64 v[92:93], v[106:107], 0, s[12:13]
	v_cvt_pk_bf16_f32 v86, v24, v25
	v_mov_b32_dpp v90, v89 quad_perm:[2,3,0,1] row_mask:0xf bank_mask:0xf bound_ctrl:1
	v_max_f32_e32 v90, v90, v90
	v_max_f32_e32 v89, v89, v90
	v_cvt_pk_bf16_f32 v87, v26, v27
	v_cvt_pk_bf16_f32 v88, v20, v21
	v_mov_b32_dpp v90, v89 row_half_mirror row_mask:0xf bank_mask:0xf bound_ctrl:1
	v_max_f32_e32 v90, v90, v90
	v_max_f32_e32 v89, v89, v90
	s_lshl_b64 s[6:7], s[10:11], 10
	s_nop 0
	v_mov_b32_dpp v90, v89 row_mirror row_mask:0xf bank_mask:0xf bound_ctrl:1
	v_max_f32_e32 v90, v90, v90
	v_max_f32_e32 v90, v89, v90
	ds_swizzle_b32 v91, v90 offset:swizzle(SWAP,16)
	v_cvt_pk_bf16_f32 v89, v22, v23
	global_store_dwordx4 v[92:93], v[86:89], off
	s_waitcnt lgkmcnt(0)
	s_nop 0
	v_max_f32_e32 v86, v91, v91
	v_max_f32_e32 v86, v90, v86
	v_mov_b32_e32 v87, v86
	s_nop 1
	v_permlane32_swap_b32_e32 v86, v87
	v_max_f32_e32 v87, v87, v87
	v_max_f32_e32 v86, v86, v86
	v_max_f32_e32 v86, v86, v87
	v_mul_f32_e32 v87, 0x3c010204, v86
	v_cmp_lt_f32_e32 vcc, 0, v86
	v_cvt_pk_bf16_f32 v88, v66, v67
	v_cvt_pk_bf16_f32 v89, v68, v69
	v_cndmask_b32_e32 v86, 1.0, v87, vcc
	v_div_scale_f32 v87, s[12:13], v86, v86, 1.0
	v_rcp_f32_e32 v146, v87
	v_cvt_pk_bf16_f32 v90, v62, v63
	v_cvt_pk_bf16_f32 v91, v64, v65
	global_store_dwordx4 v[92:93], v[88:91], off offset:1024
	s_nop 1
	v_fma_f32 v88, -v87, v146, 1.0
	v_fmac_f32_e32 v146, v88, v146
	v_div_scale_f32 v88, vcc, 1.0, v86, 1.0
	v_mul_f32_e32 v89, v88, v146
	v_fma_f32 v90, -v87, v89, v88
	v_fmac_f32_e32 v89, v90, v146
	v_fma_f32 v87, -v87, v89, v88
	v_div_fmas_f32 v87, v87, v146, v89
	v_div_fixup_f32 v87, v87, v86, 1.0
	v_fmaak_f32 v90, v24, v87, 0x4b400000
	v_fmaak_f32 v91, v25, v87, 0x4b400000
	v_fmaak_f32 v92, v26, v87, 0x4b400000
	v_fmaak_f32 v93, v27, v87, 0x4b400000
	v_perm_b32 v92, v93, v92, s61
	v_perm_b32 v90, v91, v90, s61
	v_perm_b32 v90, v92, v90, s79
	v_fmaak_f32 v91, v20, v87, 0x4b400000
	v_fmaak_f32 v92, v21, v87, 0x4b400000
	v_fmaak_f32 v93, v22, v87, 0x4b400000
	v_fmaak_f32 v146, v23, v87, 0x4b400000
	v_perm_b32 v93, v146, v93, s61
	v_perm_b32 v91, v92, v91, s61
	v_lshl_add_u64 v[88:89], v[108:109], 0, s[6:7]
	v_perm_b32 v91, v93, v91, s79
	global_store_dwordx2 v[88:89], v[90:91], off
	v_fmaak_f32 v90, v66, v87, 0x4b400000
	v_fmaak_f32 v91, v67, v87, 0x4b400000
	v_fmaak_f32 v92, v68, v87, 0x4b400000
	v_fmaak_f32 v93, v69, v87, 0x4b400000
	v_perm_b32 v92, v93, v92, s61
	v_perm_b32 v90, v91, v90, s61
	v_perm_b32 v90, v92, v90, s79
	v_fmaak_f32 v91, v62, v87, 0x4b400000
	v_fmaak_f32 v92, v63, v87, 0x4b400000
	v_fmaak_f32 v93, v64, v87, 0x4b400000
	v_fmaak_f32 v87, v65, v87, 0x4b400000
	v_perm_b32 v87, v87, v93, s61
	v_perm_b32 v91, v92, v91, s61
	v_perm_b32 v91, v87, v91, s79
	global_store_dwordx2 v[88:89], v[90:91], off offset:512
	s_and_saveexec_b64 s[6:7], s[4:5]
	s_cbranch_execz .LBB0_710
	s_lshl_b64 s[12:13], s[10:11], 2
	v_readlane_b32 s14, v254, 11
	v_readlane_b32 s15, v254, 12
	s_add_u32 s12, s14, s12
	s_addc_u32 s13, s15, s13
	global_store_dword v33, v86, s[12:13]
